# dense-attention unit prologues: all query-row load batches issued together (later batches into dead registers, moved into place), one memory round trip per unit instead of two or three
# baseline (speedup 1.0000x reference)
; #define SBAR() __builtin_amdgcn_sched_barrier(0)
; template <int NKS, bool MACC>
; __device__ __forceinline__ void attn_dense8_dma(int wv, const D8Args a, LAS unsigned char* ldsl) {
;     ...
;     const unsigned char* ksrc; const unsigned char* vsrc; const unsigned char* rsrc = nullptr;
;     { const int ri = 8 * wid + (lane >> 3), hk = (ri >> 2) & 1, ka = 32 * hk + (ri & 3) + 4 * ((ri >> 3) & 3) + 16 * (ri >> 5), kch = ((lane & 7) ^ (ri >> 1)) & 7;
;       ksrc = a.K8 + (long)ka * a.ldk + kch * 16;
;       const int vc = 16 * wid + (lane >> 2), vp = ((lane & 3) ^ (vc >> 2)) & 3; vsrc = a.Vt8 + (long)vc * a.ldvt + vp * 16;
;       if constexpr (NKS == 3) { const int rr = 16 * (wid & 3) + (lane >> 2), rh = (rr >> 2) & 1, ra = 32 * rh + (rr & 3) + 4 * ((rr >> 3) & 3) + 16 * (rr >> 5), rch = ((lane & 3) ^ (rr >> 2)) & 3;
;           rsrc = a.Kr8 + (long)ra * 64 + rch * 16; } }
;     ...
;     D8_DMA2(0, 0); D8_DMA2(128, 1); SBAR();
;     { const bf16_t* Qw = a.Q + (long)(wid * 32 + r32) * a.ldq;
; #pragma unroll
;       for (int sK = 0; sK < 2; ++sK) { const bf16_t* qp = Qw + 64 * sK + 32 * hi; unsigned w[8];
; #pragma unroll
;           for (int c = 0; c < 4; ++c) { const u32x4 v = *(const u32x4*)(qp + 8 * c);
;               w[2 * c] = pk4_fp8(bflo(v.x) * QC, bfhi(v.x) * QC, bflo(v.y) * QC, bfhi(v.y) * QC); w[2 * c + 1] = pk4_fp8(bflo(v.z) * QC, bfhi(v.z) * QC, bflo(v.w) * QC, bfhi(v.w) * QC); }
;           qf[sK] = (i32x8){(int)w[0], (int)w[1], (int)w[2], (int)w[3], (int)w[4], (int)w[5], (int)w[6], (int)w[7]}; }
; __global__ void __launch_bounds__(NTHR, 2) fwd(Params p) {
;     ...
;                 for (int u = vcu; u < 1024; u += G) {
;                     __syncthreads();
;                     const int b = u >> 7, qb = u & 15, h = (u >> 4) & 7;
;                     if constexpr (F8_ATTD) {
;                         d8::D8Args a; a.Q = Qd + (size_t)(b * SEQ + 256 * qb) * 1536 + h * 192; a.ldq = 1536;
;                         a.K8 = ws + WS_WGU1 + 64 * MiB + (size_t)b * SEQ * 1024 + h * 128; a.ldk = 1024; a.Kr8 = ws + WS_WD1 + 32 * MiB + (size_t)b * SEQ * 64;
;                         a.Vt8 = ws + WS_WGU1 + 96 * MiB + (size_t)(b * 8 + h) * 128 * SEQ; a.ldvt = SEQ;
;                         { const size_t eo = (size_t)(b * SEQ + 256 * qb) * DM + 1024 + h * 128; a.O = F8_OUT ? (bf16_t*)((unsigned char*)Oat + eo) : Oat + eo; } a.ldo = DM; a.seq = SEQ; a.pos0 = 256 * qb;
.LBB0_455:
	s_ashr_i32 s24, s54, 7
	s_lshl_b32 s1, s54, 8
	s_lshl_b32 s0, s24, 12
	s_and_b32 s23, s1, 0xf00
	s_or_b32 s34, s0, s23
	s_bfe_u32 s33, s54, 0x30004
	s_mul_i32 s1, s34, 0xc00
	s_mul_hi_i32 s0, s34, 0xc00
	s_add_u32 s1, s44, s1
	s_addc_u32 s2, s45, s0
	s_mul_i32 s0, s33, 0x180
	s_add_u32 s0, s1, s0
	s_addc_u32 s1, s2, 0
	s_ashr_i32 s25, s24, 31
	s_lshl_b64 s[2:3], s[24:25], 22
	s_add_u32 s15, s6, s2
	s_addc_u32 s29, s7, s3
	s_lshl_b32 s55, s33, 7
	s_add_u32 s28, s15, s55
	s_addc_u32 s29, s29, 0
	s_lshl_b64 s[42:43], s[24:25], 18
	s_add_u32 s40, s8, s42
	s_addc_u32 s41, s9, s43
	s_lshl_b32 s15, s24, 3
	s_or_b32 s24, s15, s33
	s_ashr_i32 s25, s24, 31
	s_waitcnt vmcnt(0)
	s_barrier
	s_lshl_b64 s[24:25], s[24:25], 19
	v_mbcnt_lo_u32_b32 v32, -1, 0
	v_mbcnt_hi_u32_b32 v32, -1, v32
	s_add_u32 s24, s52, s24
	v_add_u32_e32 v0, s5, v32
	s_addc_u32 s25, s53, s25
	v_readfirstlane_b32 s35, v0
	s_ashr_i32 s33, s35, 6
	s_lshl_b32 s49, s33, 2
	s_lshl_b32 s48, s33, 3
	v_bfe_u32 v0, v32, 3, 3
	s_and_b32 s59, s49, 12
	s_ashr_i32 s49, s35, 4
	v_and_b32_e32 v48, 63, v32
	v_or_b32_e32 v1, s48, v0
	v_and_b32_e32 v33, 32, v32
	s_and_b32 s49, s49, -16
	v_bfe_u32 v65, v48, 3, 2
	v_add_u32_e32 v71, s49, v33
	v_lshrrev_b32_e32 v1, 1, v1
	v_or3_b32 v0, v65, s59, v71
	v_xor_b32_e32 v2, v1, v32
	v_ashrrev_i32_e32 v1, 31, v0
	v_lshlrev_b32_e32 v2, 4, v2
	s_lshl_b32 s60, s33, 4
	v_bfe_u32 v70, v32, 2, 4
	v_lshlrev_b64 v[0:1], 10, v[0:1]
	v_and_b32_e32 v232, 0x70, v2
	v_or_b32_e32 v2, s60, v70
	v_lshl_add_u64 v[0:1], s[28:29], 0, v[0:1]
	v_ashrrev_i32_e32 v3, 31, v2
	s_and_b32 s28, s33, 3
	v_lshlrev_b64 v[2:3], 12, v[2:3]
	v_lshlrev_b32_e32 v4, 4, v32
	s_lshl_b32 s61, s28, 4
	v_lshl_add_u64 v[2:3], s[24:25], 0, v[2:3]
	v_bitop3_b32 v66, v4, 48, v32 bitop3:0x48
	v_mov_b32_e32 v67, v233
	v_or_b32_e32 v4, s61, v70
	v_lshl_add_u64 v[2:3], v[2:3], 0, v[66:67]
	v_lshlrev_b32_e32 v6, 1, v32
	v_bfe_u32 v67, v48, 2, 2
	v_lshrrev_b32_e32 v4, 1, v4
	s_and_b32 s62, s48, 16
	v_lshrrev_b32_e32 v5, 4, v32
	v_and_b32_e32 v6, 32, v6
	v_and_b32_e32 v4, 12, v4
	v_or_b32_e32 v7, s62, v67
	v_or3_b32 v4, v7, v4, v6
	v_xor_b32_e32 v6, v5, v32
	s_lshl_b32 s24, s33, 10
	v_lshl_add_u64 v[0:1], v[0:1], 0, v[232:233]
	v_lshlrev_b32_e32 v6, 4, v6
	s_add_i32 s56, s24, 0
	s_mov_b64 s[24:25], 0x10000
	s_ashr_i32 s29, s35, 8
	v_and_b32_e32 v68, 48, v6
	v_lshl_add_u64 v[6:7], v[0:1], 0, s[24:25]
	s_lshl_b32 s24, s29, 6
	s_add_i32 s57, s56, 0x12000
	s_mov_b32 m0, s56
	s_ashr_i32 s25, s24, 31
	v_lshlrev_b32_e32 v4, 6, v4
	v_mov_b32_e32 v5, v233
	global_load_lds_dwordx4 v[0:1], off
	s_mov_b32 m0, s57
	s_lshl_b64 s[72:73], s[24:25], 6
	s_lshl_b32 s24, s29, 12
	v_mov_b32_e32 v69, v233
	global_load_lds_dwordx4 v[2:3], off
	s_add_i32 m0, s56, 0x2000
	v_lshl_add_u64 v[4:5], s[40:41], 0, v[4:5]
	s_add_i32 s58, s24, 0
	s_lshl_b32 s24, s28, 10
	global_load_lds_dwordx4 v[6:7], off
	v_lshl_add_u64 v[6:7], v[2:3], 0, 64
	s_add_i32 m0, s56, 0x14000
	v_lshl_add_u64 v[4:5], v[4:5], 0, v[68:69]
	s_add_i32 s58, s58, s24
	global_load_lds_dwordx4 v[6:7], off
	v_lshl_add_u64 v[4:5], v[4:5], 0, s[72:73]
	s_add_i32 m0, s58, 0xc000
	v_lshl_add_u64 v[6:7], v[0:1], 0, s[26:27]
	global_load_lds_dwordx4 v[4:5], off
	s_add_i32 m0, s56, 0x4000
	s_mov_b64 s[24:25], 0x30000
	global_load_lds_dwordx4 v[6:7], off
	v_lshl_add_u64 v[6:7], v[2:3], 0, s[20:21]
	s_add_i32 m0, s56, 0x16000
	v_lshl_add_u64 v[0:1], v[0:1], 0, s[24:25]
	global_load_lds_dwordx4 v[6:7], off
	s_add_i32 m0, s56, 0x6000
	s_mov_b64 s[24:25], 0xc0
	global_load_lds_dwordx4 v[0:1], off
	v_lshl_add_u64 v[0:1], v[2:3], 0, s[24:25]
	s_add_i32 m0, s56, 0x18000
	s_mov_b64 s[24:25], 0x2000
	global_load_lds_dwordx4 v[0:1], off
	v_lshl_add_u64 v[0:1], v[4:5], 0, s[24:25]
	s_add_i32 m0, s58, 0xe000
	v_and_b32_e32 v72, 31, v32
	global_load_lds_dwordx4 v[0:1], off
	s_lshl_b32 s24, s33, 5
	v_or_b32_e32 v2, s24, v72
	v_mov_b64_e32 v[0:1], s[0:1]
	s_movk_i32 s0, 0xc00
	v_mad_i64_i32 v[12:13], s[0:1], v2, s0, v[0:1]
	v_lshlrev_b32_e32 v0, 1, v33
	v_mov_b32_e32 v1, v233
	v_lshl_add_u64 v[22:23], v[12:13], 0, v[0:1]
	global_load_dwordx4 v[4:7], v[22:23], off
	global_load_dwordx4 v[8:11], v[22:23], off offset:16
	global_load_dwordx4 v[14:17], v[22:23], off offset:32
	global_load_dwordx4 v[18:21], v[22:23], off offset:48
	global_load_dwordx4 v[0:3], v[22:23], off offset:176
	global_load_dwordx4 v[34:37], v[22:23], off offset:160
	global_load_dwordx4 v[38:41], v[22:23], off offset:144
	global_load_dwordx4 v[42:45], v[22:23], off offset:128
	global_load_dwordx4 v[112:115], v[12:13], off offset:336
	global_load_dwordx4 v[116:119], v[12:13], off offset:320
	global_load_dwordx4 v[120:123], v[12:13], off offset:272
	global_load_dwordx4 v[124:127], v[12:13], off offset:256
	global_load_dwordx4 v[56:59], v[12:13], off offset:304
	global_load_dwordx4 v[60:63], v[12:13], off offset:288
	global_load_dwordx4 v[74:77], v[12:13], off offset:368
	global_load_dwordx4 v[78:81], v[12:13], off offset:352
	v_cmp_gt_u32_e64 s[40:41], 32, v48
	s_waitcnt vmcnt(0)
; __device__ __forceinline__ float bflo(unsigned w) { return __uint_as_float(w << 16); }
; __device__ __forceinline__ float bfhi(unsigned w) { return __uint_as_float(w & 0xffff0000u); }
; template <int NKS, bool MACC>
; __device__ __forceinline__ void attn_dense8_dma(int wv, const D8Args a, LAS unsigned char* ldsl) {
;     ...
;     { const bf16_t* Qw = a.Q + (long)(wid * 32 + r32) * a.ldq;
; #pragma unroll
;       for (int sK = 0; sK < 2; ++sK) { const bf16_t* qp = Qw + 64 * sK + 32 * hi; unsigned w[8];
; #pragma unroll
;           for (int c = 0; c < 4; ++c) { const u32x4 v = *(const u32x4*)(qp + 8 * c);
;               w[2 * c] = pk4_fp8(bflo(v.x) * QC, bfhi(v.x) * QC, bflo(v.y) * QC, bfhi(v.y) * QC); w[2 * c + 1] = pk4_fp8(bflo(v.z) * QC, bfhi(v.z) * QC, bflo(v.w) * QC, bfhi(v.w) * QC); }
;           qf[sK] = (i32x8){(int)w[0], (int)w[1], (int)w[2], (int)w[3], (int)w[4], (int)w[5], (int)w[6], (int)w[7]}; }
	v_lshlrev_b32_e32 v22, 16, v4
	v_and_b32_e32 v4, 0xffff0000, v4
	v_lshlrev_b32_e32 v24, 16, v6
	v_and_b32_e32 v6, 0xffff0000, v6
	v_lshlrev_b32_e32 v26, 16, v8
	v_and_b32_e32 v8, 0xffff0000, v8
	v_lshlrev_b32_e32 v28, 16, v10
	v_and_b32_e32 v10, 0xffff0000, v10
	v_lshlrev_b32_e32 v30, 16, v14
	v_and_b32_e32 v14, 0xffff0000, v14
	v_lshlrev_b32_e32 v46, 16, v16
	v_and_b32_e32 v16, 0xffff0000, v16
	v_lshlrev_b32_e32 v49, 16, v18
	v_and_b32_e32 v18, 0xffff0000, v18
	v_mul_f32_e32 v176, 0x3dd53b94, v22
	v_mul_f32_e32 v4, 0x3dd53b94, v4
	v_mul_f32_e32 v177, 0x3dd53b94, v24
	v_mul_f32_e32 v6, 0x3dd53b94, v6
	v_mul_f32_e32 v178, 0x3dd53b94, v26
	v_mul_f32_e32 v8, 0x3dd53b94, v8
	v_mul_f32_e32 v179, 0x3dd53b94, v28
	v_mul_f32_e32 v10, 0x3dd53b94, v10
	v_mul_f32_e32 v180, 0x3dd53b94, v30
	v_mul_f32_e32 v14, 0x3dd53b94, v14
	v_mul_f32_e32 v181, 0x3dd53b94, v46
	v_mul_f32_e32 v16, 0x3dd53b94, v16
	v_mul_f32_e32 v182, 0x3dd53b94, v49
	v_mul_f32_e32 v18, 0x3dd53b94, v18
	v_cvt_pk_fp8_f32 v176, v176, v4
	v_cvt_pk_fp8_f32 v177, v177, v6
	v_cvt_pk_fp8_f32 v178, v178, v8
	v_cvt_pk_fp8_f32 v179, v179, v10
	v_cvt_pk_fp8_f32 v180, v180, v14
	v_cvt_pk_fp8_f32 v181, v181, v16
	v_cvt_pk_fp8_f32 v182, v182, v18
	v_lshlrev_b32_e32 v23, 16, v5
	v_and_b32_e32 v5, 0xffff0000, v5
	v_lshlrev_b32_e32 v25, 16, v7
	v_and_b32_e32 v7, 0xffff0000, v7
	v_lshlrev_b32_e32 v27, 16, v9
	v_and_b32_e32 v9, 0xffff0000, v9
	v_lshlrev_b32_e32 v29, 16, v11
	v_and_b32_e32 v11, 0xffff0000, v11
	v_lshlrev_b32_e32 v31, 16, v15
	v_and_b32_e32 v15, 0xffff0000, v15
	v_lshlrev_b32_e32 v47, 16, v17
	v_and_b32_e32 v17, 0xffff0000, v17
	v_lshlrev_b32_e32 v50, 16, v19
	v_and_b32_e32 v19, 0xffff0000, v19
	v_lshlrev_b32_e32 v51, 16, v20
	v_and_b32_e32 v20, 0xffff0000, v20
	v_mul_f32_e32 v22, 0x3dd53b94, v23
	v_mul_f32_e32 v5, 0x3dd53b94, v5
	v_mul_f32_e32 v23, 0x3dd53b94, v25
	v_mul_f32_e32 v7, 0x3dd53b94, v7
	v_mul_f32_e32 v24, 0x3dd53b94, v27
	v_mul_f32_e32 v9, 0x3dd53b94, v9
	v_mul_f32_e32 v25, 0x3dd53b94, v29
	v_mul_f32_e32 v11, 0x3dd53b94, v11
	v_mul_f32_e32 v26, 0x3dd53b94, v31
	v_mul_f32_e32 v15, 0x3dd53b94, v15
	v_mul_f32_e32 v27, 0x3dd53b94, v47
	v_mul_f32_e32 v17, 0x3dd53b94, v17
	v_mul_f32_e32 v28, 0x3dd53b94, v50
	v_mul_f32_e32 v19, 0x3dd53b94, v19
	v_mul_f32_e32 v183, 0x3dd53b94, v51
	v_mul_f32_e32 v20, 0x3dd53b94, v20
	v_lshlrev_b32_e32 v52, 16, v21
	v_cvt_pk_fp8_f32 v176, v22, v5 op_sel:[0,0,1]
	v_cvt_pk_fp8_f32 v177, v23, v7 op_sel:[0,0,1]
	v_cvt_pk_fp8_f32 v178, v24, v9 op_sel:[0,0,1]
	v_cvt_pk_fp8_f32 v179, v25, v11 op_sel:[0,0,1]
	v_cvt_pk_fp8_f32 v180, v26, v15 op_sel:[0,0,1]
	v_cvt_pk_fp8_f32 v181, v27, v17 op_sel:[0,0,1]
	v_cvt_pk_fp8_f32 v182, v28, v19 op_sel:[0,0,1]
	v_cvt_pk_fp8_f32 v183, v183, v20
	v_and_b32_e32 v5, 0xffff0000, v21
	v_mov_b64_e32 v[16:17], v[112:113]
	v_mov_b64_e32 v[18:19], v[114:115]
	v_mov_b64_e32 v[24:25], v[116:117]
	v_mov_b64_e32 v[26:27], v[118:119]
	v_mov_b64_e32 v[20:21], v[120:121]
	v_mov_b64_e32 v[22:23], v[122:123]
	v_mov_b64_e32 v[28:29], v[124:125]
	v_mov_b64_e32 v[30:31], v[126:127]
	v_mul_f32_e32 v4, 0x3dd53b94, v52
	v_mul_f32_e32 v5, 0x3dd53b94, v5
	v_cvt_pk_fp8_f32 v183, v4, v5 op_sel:[0,0,1]
	v_lshlrev_b32_e32 v4, 16, v42
	v_mul_f32_e32 v184, 0x3dd53b94, v4
	v_and_b32_e32 v4, 0xffff0000, v42
	v_mul_f32_e32 v4, 0x3dd53b94, v4
	v_cvt_pk_fp8_f32 v184, v184, v4
	v_lshlrev_b32_e32 v5, 16, v43
	v_mul_f32_e32 v4, 0x3dd53b94, v5
	v_and_b32_e32 v5, 0xffff0000, v43
	v_mul_f32_e32 v5, 0x3dd53b94, v5
	v_cvt_pk_fp8_f32 v184, v4, v5 op_sel:[0,0,1]
	v_lshlrev_b32_e32 v4, 16, v44
	v_mul_f32_e32 v185, 0x3dd53b94, v4
	v_and_b32_e32 v4, 0xffff0000, v44
	v_mul_f32_e32 v4, 0x3dd53b94, v4
	v_cvt_pk_fp8_f32 v185, v185, v4
	v_lshlrev_b32_e32 v5, 16, v45
	v_mul_f32_e32 v4, 0x3dd53b94, v5
	v_and_b32_e32 v5, 0xffff0000, v45
	v_mul_f32_e32 v5, 0x3dd53b94, v5
	v_cvt_pk_fp8_f32 v185, v4, v5 op_sel:[0,0,1]
	v_lshlrev_b32_e32 v4, 16, v38
	v_mul_f32_e32 v186, 0x3dd53b94, v4
	v_and_b32_e32 v4, 0xffff0000, v38
	v_mul_f32_e32 v4, 0x3dd53b94, v4
	v_cvt_pk_fp8_f32 v186, v186, v4
	v_lshlrev_b32_e32 v5, 16, v39
	v_mul_f32_e32 v4, 0x3dd53b94, v5
	v_and_b32_e32 v5, 0xffff0000, v39
	v_mul_f32_e32 v5, 0x3dd53b94, v5
	v_cvt_pk_fp8_f32 v186, v4, v5 op_sel:[0,0,1]
	v_lshlrev_b32_e32 v4, 16, v40
	v_mul_f32_e32 v187, 0x3dd53b94, v4
	v_and_b32_e32 v4, 0xffff0000, v40
	v_mul_f32_e32 v4, 0x3dd53b94, v4
	v_cvt_pk_fp8_f32 v187, v187, v4
	v_lshlrev_b32_e32 v5, 16, v41
	v_mul_f32_e32 v4, 0x3dd53b94, v5
	v_and_b32_e32 v5, 0xffff0000, v41
	v_mul_f32_e32 v5, 0x3dd53b94, v5
	v_cvt_pk_fp8_f32 v187, v4, v5 op_sel:[0,0,1]
	v_lshlrev_b32_e32 v4, 16, v34
	v_mul_f32_e32 v188, 0x3dd53b94, v4
	v_and_b32_e32 v4, 0xffff0000, v34
	v_mul_f32_e32 v4, 0x3dd53b94, v4
	v_cvt_pk_fp8_f32 v188, v188, v4
	v_lshlrev_b32_e32 v5, 16, v35
	v_mul_f32_e32 v4, 0x3dd53b94, v5
	v_and_b32_e32 v5, 0xffff0000, v35
	v_mul_f32_e32 v5, 0x3dd53b94, v5
	v_cvt_pk_fp8_f32 v188, v4, v5 op_sel:[0,0,1]
	v_lshlrev_b32_e32 v4, 16, v36
	v_mul_f32_e32 v189, 0x3dd53b94, v4
	v_and_b32_e32 v4, 0xffff0000, v36
	v_mul_f32_e32 v4, 0x3dd53b94, v4
	v_cvt_pk_fp8_f32 v189, v189, v4
	v_lshlrev_b32_e32 v5, 16, v37
	v_mul_f32_e32 v4, 0x3dd53b94, v5
	v_and_b32_e32 v5, 0xffff0000, v37
	v_mul_f32_e32 v5, 0x3dd53b94, v5
	v_cvt_pk_fp8_f32 v189, v4, v5 op_sel:[0,0,1]
	v_lshlrev_b32_e32 v4, 16, v0
	v_and_b32_e32 v0, 0xffff0000, v0
	v_mul_f32_e32 v190, 0x3dd53b94, v4
	v_mul_f32_e32 v0, 0x3dd53b94, v0
	v_cvt_pk_fp8_f32 v190, v190, v0
	v_lshlrev_b32_e32 v4, 16, v1
	v_and_b32_e32 v1, 0xffff0000, v1
	v_mul_f32_e32 v0, 0x3dd53b94, v4
	v_mul_f32_e32 v1, 0x3dd53b94, v1
	v_cvt_pk_fp8_f32 v190, v0, v1 op_sel:[0,0,1]
	v_lshlrev_b32_e32 v0, 16, v2
	v_mul_f32_e32 v191, 0x3dd53b94, v0
	v_and_b32_e32 v0, 0xffff0000, v2
	v_mul_f32_e32 v0, 0x3dd53b94, v0
	v_cvt_pk_fp8_f32 v191, v191, v0
	v_or_b32_e32 v0, s23, v72
	v_add_u32_e32 v0, s24, v0
	v_cvt_f32_i32_e32 v34, v0
	s_waitcnt vmcnt(0)
; __device__ __forceinline__ float bflo(unsigned w) { return __uint_as_float(w << 16); }
; __device__ __forceinline__ float bfhi(unsigned w) { return __uint_as_float(w & 0xffff0000u); }
; __device__ __forceinline__ float inv_freq32(int i) { return __builtin_amdgcn_exp2f(-(float)i * 0.41524101186092029f); }
; template <int NKS, bool MACC>
; __device__ __forceinline__ void attn_dense8_dma(int wv, const D8Args a, LAS unsigned char* ldsl) {
;     ...
;       if constexpr (NKS == 3) {
;           const float pos = (float)(a.pos0 + wid * 32 + r32); const bf16_t* qp = Qw + 128; unsigned w[8];
; #pragma unroll
;           for (int c = 0; c < 4; ++c) { const u32x4 v1 = *(const u32x4*)(qp + 8 * c), v2 = *(const u32x4*)(qp + 32 + 8 * c);
;               const unsigned a1[4] = {v1.x, v1.y, v1.z, v1.w}, a2[4] = {v2.x, v2.y, v2.z, v2.w}; float y[8];
; #pragma unroll
;               for (int e = 0; e < 8; ++e) { const int i = 8 * c + e; float sn, cs; sincos_rev(pos * inv_freq32(i), sn, cs);
;                   const float x1 = (e & 1) ? bfhi(a1[e >> 1]) : bflo(a1[e >> 1]), x2 = (e & 1) ? bfhi(a2[e >> 1]) : bflo(a2[e >> 1]);
;                   y[e] = (hi ? (x2 * cs + x1 * sn) : (x1 * cs - x2 * sn)) * QC; }
;               w[2 * c] = pk4_fp8(y[0], y[1], y[2], y[3]); w[2 * c + 1] = pk4_fp8(y[4], y[5], y[6], y[7]); }
	v_lshlrev_b32_e32 v39, 16, v24
	v_lshlrev_b32_e32 v38, 16, v28
	v_lshlrev_b32_e32 v1, 16, v3
	v_mul_f32_e32 v4, 0.15915494, v34
	v_floor_f32_e32 v4, v4
	v_fma_f32 v4, v34, 0.15915494, -v4
	v_sin_f32_e32 v36, v4
	v_cos_f32_e32 v37, v4
	v_and_b32_e32 v2, 0xffff0000, v3
	v_mul_f32_e32 v1, 0x3dd53b94, v1
	v_mul_f32_e32 v2, 0x3dd53b94, v2
	v_pk_mul_f32 v[40:41], v[36:37], v[38:39]
	v_cvt_pk_fp8_f32 v191, v1, v2 op_sel:[0,0,1]
	v_add_f32_e32 v35, v40, v41
	v_mov_b32_e32 v40, v37
	v_mov_b32_e32 v41, v36
	v_pk_mul_f32 v[36:37], v[40:41], v[38:39]
	v_and_b32_e32 v39, 0xffff0000, v24
	v_sub_f32_e32 v36, v36, v37
	v_cndmask_b32_e64 v35, v35, v36, s[40:41]
	v_exp_f32_e32 v36, 0xbed49a78
	v_and_b32_e32 v38, 0xffff0000, v28
	v_mul_f32_e32 v192, 0x3dd53b94, v35
	v_mov_b64_e32 v[0:1], v[56:57]
	v_mov_b64_e32 v[2:3], v[58:59]
	v_mov_b64_e32 v[8:9], v[60:61]
	v_mov_b64_e32 v[10:11], v[62:63]
	v_mul_f32_e32 v36, v36, v34
	v_mul_f32_e32 v37, 0.15915494, v36
	v_floor_f32_e32 v37, v37
	v_fma_f32 v37, v36, 0.15915494, -v37
	v_sin_f32_e32 v36, v37
	v_cos_f32_e32 v37, v37
	v_mov_b64_e32 v[4:5], v[74:75]
	v_mov_b64_e32 v[6:7], v[76:77]
	v_mov_b64_e32 v[12:13], v[78:79]
	v_mov_b64_e32 v[14:15], v[80:81]
	v_pk_mul_f32 v[40:41], v[36:37], v[38:39]
	s_nop 0
	v_add_f32_e32 v24, v40, v41
	v_mov_b32_e32 v40, v37
	v_mov_b32_e32 v41, v36
	v_pk_mul_f32 v[36:37], v[40:41], v[38:39]
	v_lshlrev_b32_e32 v39, 16, v25
	v_sub_f32_e32 v28, v36, v37
	v_cndmask_b32_e64 v24, v24, v28, s[40:41]
	v_exp_f32_e32 v28, 0xbf549a78
	v_lshlrev_b32_e32 v38, 16, v29
	v_and_b32_e32 v25, 0xffff0000, v25
	v_mul_f32_e32 v28, v28, v34
	v_mul_f32_e32 v35, 0.15915494, v28
	v_floor_f32_e32 v35, v35
	v_fma_f32 v28, v28, 0.15915494, -v35
	v_sin_f32_e32 v36, v28
	v_cos_f32_e32 v37, v28
	v_mul_f32_e32 v35, 0x3dd53b94, v24
	v_cvt_pk_fp8_f32 v192, v192, v35
	v_pk_mul_f32 v[40:41], v[36:37], v[38:39]
	s_nop 0
	v_add_f32_e32 v24, v40, v41
	v_mov_b32_e32 v40, v37
	v_mov_b32_e32 v41, v36
	v_pk_mul_f32 v[36:37], v[40:41], v[38:39]
	s_nop 0
	v_sub_f32_e32 v28, v36, v37
	v_cndmask_b32_e64 v24, v24, v28, s[40:41]
	v_exp_f32_e32 v28, 0xbf9f73da
	v_mul_f32_e32 v38, 0x3dd53b94, v24
	v_and_b32_e32 v24, 0xffff0000, v29
	v_mul_f32_e32 v28, v28, v34
	v_mul_f32_e32 v36, 0.15915494, v28
	v_floor_f32_e32 v36, v36
	v_fma_f32 v28, v28, 0.15915494, -v36
	v_sin_f32_e32 v36, v28
	v_cos_f32_e32 v37, v28
	s_nop 0
	v_pk_mul_f32 v[28:29], v[36:37], v[24:25]
	s_nop 0
	v_add_f32_e32 v39, v28, v29
	v_mov_b32_e32 v28, v37
	v_mov_b32_e32 v29, v36
	v_pk_mul_f32 v[24:25], v[28:29], v[24:25]
	v_lshlrev_b32_e32 v29, 16, v26
	v_sub_f32_e32 v24, v24, v25
	v_cndmask_b32_e64 v28, v39, v24, s[40:41]
	v_exp_f32_e32 v24, 0xbfd49a78
	v_mul_f32_e32 v39, 0x3dd53b94, v28
	v_lshlrev_b32_e32 v28, 16, v30
	v_cvt_pk_fp8_f32 v192, v38, v39 op_sel:[0,0,1]
	v_mul_f32_e32 v24, v24, v34
	v_mul_f32_e32 v25, 0.15915494, v24
	v_floor_f32_e32 v25, v25
	v_fma_f32 v25, v24, 0.15915494, -v25
	v_sin_f32_e32 v24, v25
	v_cos_f32_e32 v25, v25
	s_nop 0
	v_pk_mul_f32 v[36:37], v[24:25], v[28:29]
	s_nop 0
	v_add_f32_e32 v40, v36, v37
	v_mov_b32_e32 v36, v25
	v_mov_b32_e32 v37, v24
	v_pk_mul_f32 v[24:25], v[36:37], v[28:29]
	v_and_b32_e32 v29, 0xffff0000, v26
	v_sub_f32_e32 v24, v24, v25
	v_cndmask_b32_e64 v28, v40, v24, s[40:41]
	v_exp_f32_e32 v24, 0xc004e08b
	v_mul_f32_e32 v193, 0x3dd53b94, v28
	v_and_b32_e32 v28, 0xffff0000, v30
	v_mul_f32_e32 v24, v24, v34
	v_mul_f32_e32 v25, 0.15915494, v24
	v_floor_f32_e32 v25, v25
	v_fma_f32 v25, v24, 0.15915494, -v25
	v_sin_f32_e32 v24, v25
	v_cos_f32_e32 v25, v25
	s_nop 0
	v_pk_mul_f32 v[36:37], v[24:25], v[28:29]
	s_nop 0
	v_add_f32_e32 v26, v36, v37
	v_mov_b32_e32 v36, v25
	v_mov_b32_e32 v37, v24
	v_pk_mul_f32 v[24:25], v[36:37], v[28:29]
	v_lshlrev_b32_e32 v29, 16, v27
	v_sub_f32_e32 v24, v24, v25
	v_cndmask_b32_e64 v26, v26, v24, s[40:41]
	v_exp_f32_e32 v24, 0xc01f73da
	v_lshlrev_b32_e32 v28, 16, v31
	v_mul_f32_e32 v30, 0x3dd53b94, v26
	v_and_b32_e32 v27, 0xffff0000, v27
	v_mul_f32_e32 v24, v24, v34
	v_mul_f32_e32 v25, 0.15915494, v24
	v_floor_f32_e32 v25, v25
	v_fma_f32 v25, v24, 0.15915494, -v25
	v_sin_f32_e32 v24, v25
	v_cos_f32_e32 v25, v25
	v_cvt_pk_fp8_f32 v193, v193, v30
	v_pk_mul_f32 v[36:37], v[24:25], v[28:29]
	s_nop 0
	v_add_f32_e32 v26, v36, v37
	v_mov_b32_e32 v36, v25
	v_mov_b32_e32 v37, v24
	v_pk_mul_f32 v[24:25], v[36:37], v[28:29]
	s_nop 0
	v_sub_f32_e32 v24, v24, v25
	v_cndmask_b32_e64 v26, v26, v24, s[40:41]
	v_exp_f32_e32 v24, 0xc03a0729
	v_mul_f32_e32 v36, 0x3dd53b94, v26
	v_and_b32_e32 v26, 0xffff0000, v31
	v_mul_f32_e32 v24, v24, v34
	v_mul_f32_e32 v25, 0.15915494, v24
	v_floor_f32_e32 v25, v25
	v_fma_f32 v25, v24, 0.15915494, -v25
	v_sin_f32_e32 v24, v25
	v_cos_f32_e32 v25, v25
	s_nop 0
	v_pk_mul_f32 v[28:29], v[24:25], v[26:27]
	s_nop 0
	v_add_f32_e32 v31, v28, v29
	v_mov_b32_e32 v28, v25
	v_mov_b32_e32 v29, v24
	v_pk_mul_f32 v[24:25], v[28:29], v[26:27]
	v_lshlrev_b32_e32 v27, 16, v16
	v_sub_f32_e32 v24, v24, v25
	v_cndmask_b32_e64 v24, v31, v24, s[40:41]
	v_mul_f32_e32 v26, 0x3dd53b94, v24
	v_exp_f32_e32 v24, 0xc0549a78
	v_cvt_pk_fp8_f32 v193, v36, v26 op_sel:[0,0,1]
	v_lshlrev_b32_e32 v26, 16, v20
	v_mul_f32_e32 v24, v24, v34
	v_mul_f32_e32 v25, 0.15915494, v24
	v_floor_f32_e32 v25, v25
	v_fma_f32 v25, v24, 0.15915494, -v25
	v_sin_f32_e32 v24, v25
	v_cos_f32_e32 v25, v25
	s_nop 0
	v_pk_mul_f32 v[28:29], v[24:25], v[26:27]
	s_nop 0
	v_add_f32_e32 v30, v28, v29
	v_mov_b32_e32 v28, v25
	v_mov_b32_e32 v29, v24
	v_pk_mul_f32 v[24:25], v[28:29], v[26:27]
	v_and_b32_e32 v27, 0xffff0000, v16
	v_sub_f32_e32 v24, v24, v25
	v_cndmask_b32_e64 v26, v30, v24, s[40:41]
	v_exp_f32_e32 v24, 0xc06f2dc7
; __device__ __forceinline__ float bflo(unsigned w) { return __uint_as_float(w << 16); }
; __device__ __forceinline__ float bfhi(unsigned w) { return __uint_as_float(w & 0xffff0000u); }
; __device__ __forceinline__ float inv_freq32(int i) { return __builtin_amdgcn_exp2f(-(float)i * 0.41524101186092029f); }
; template <int NKS, bool MACC>
; __device__ __forceinline__ void attn_dense8_dma(int wv, const D8Args a, LAS unsigned char* ldsl) {
;     ...
;           for (int c = 0; c < 4; ++c) { const u32x4 v1 = *(const u32x4*)(qp + 8 * c), v2 = *(const u32x4*)(qp + 32 + 8 * c);
;               const unsigned a1[4] = {v1.x, v1.y, v1.z, v1.w}, a2[4] = {v2.x, v2.y, v2.z, v2.w}; float y[8];
; #pragma unroll
;               for (int e = 0; e < 8; ++e) { const int i = 8 * c + e; float sn, cs; sincos_rev(pos * inv_freq32(i), sn, cs);
;                   const float x1 = (e & 1) ? bfhi(a1[e >> 1]) : bflo(a1[e >> 1]), x2 = (e & 1) ? bfhi(a2[e >> 1]) : bflo(a2[e >> 1]);
;                   y[e] = (hi ? (x2 * cs + x1 * sn) : (x1 * cs - x2 * sn)) * QC; }
;               w[2 * c] = pk4_fp8(y[0], y[1], y[2], y[3]); w[2 * c + 1] = pk4_fp8(y[4], y[5], y[6], y[7]); }
	v_mul_f32_e32 v194, 0x3dd53b94, v26
	v_and_b32_e32 v26, 0xffff0000, v20
	v_mul_f32_e32 v24, v24, v34
	v_mul_f32_e32 v25, 0.15915494, v24
	v_floor_f32_e32 v25, v25
	v_fma_f32 v25, v24, 0.15915494, -v25
	v_sin_f32_e32 v24, v25
	v_cos_f32_e32 v25, v25
	s_nop 0
	v_pk_mul_f32 v[28:29], v[24:25], v[26:27]
	s_nop 0
	v_add_f32_e32 v16, v28, v29
	v_mov_b32_e32 v28, v25
	v_mov_b32_e32 v29, v24
	v_pk_mul_f32 v[24:25], v[28:29], v[26:27]
	v_lshlrev_b32_e32 v27, 16, v17
	v_sub_f32_e32 v20, v24, v25
	v_cndmask_b32_e64 v16, v16, v20, s[40:41]
	v_exp_f32_e32 v20, 0xc084e08b
	v_lshlrev_b32_e32 v26, 16, v21
	v_mul_f32_e32 v30, 0x3dd53b94, v16
	v_and_b32_e32 v17, 0xffff0000, v17
	v_mul_f32_e32 v20, v20, v34
	v_mul_f32_e32 v24, 0.15915494, v20
	v_floor_f32_e32 v24, v24
	v_fma_f32 v20, v20, 0.15915494, -v24
	v_sin_f32_e32 v24, v20
	v_cos_f32_e32 v25, v20
	v_cvt_pk_fp8_f32 v194, v194, v30
	v_pk_mul_f32 v[28:29], v[24:25], v[26:27]
	s_nop 0
	v_add_f32_e32 v16, v28, v29
	v_mov_b32_e32 v28, v25
	v_mov_b32_e32 v29, v24
	v_pk_mul_f32 v[24:25], v[28:29], v[26:27]
	s_nop 0
	v_sub_f32_e32 v20, v24, v25
	v_cndmask_b32_e64 v16, v16, v20, s[40:41]
	v_exp_f32_e32 v20, 0xc0922a32
	v_mul_f32_e32 v26, 0x3dd53b94, v16
	v_and_b32_e32 v16, 0xffff0000, v21
	v_mul_f32_e32 v20, v20, v34
	v_mul_f32_e32 v24, 0.15915494, v20
	v_floor_f32_e32 v24, v24
	v_fma_f32 v20, v20, 0.15915494, -v24
	v_sin_f32_e32 v24, v20
	v_cos_f32_e32 v25, v20
	s_nop 0
	v_pk_mul_f32 v[20:21], v[24:25], v[16:17]
	s_nop 0
	v_add_f32_e32 v27, v20, v21
	v_mov_b32_e32 v20, v25
	v_mov_b32_e32 v21, v24
	v_pk_mul_f32 v[16:17], v[20:21], v[16:17]
	v_lshlrev_b32_e32 v21, 16, v18
	v_sub_f32_e32 v16, v16, v17
	v_cndmask_b32_e64 v20, v27, v16, s[40:41]
	v_exp_f32_e32 v16, 0xc09f73da
	v_mul_f32_e32 v27, 0x3dd53b94, v20
	v_lshlrev_b32_e32 v20, 16, v22
	v_cvt_pk_fp8_f32 v194, v26, v27 op_sel:[0,0,1]
	v_mul_f32_e32 v16, v16, v34
	v_mul_f32_e32 v17, 0.15915494, v16
	v_floor_f32_e32 v17, v17
	v_fma_f32 v17, v16, 0.15915494, -v17
	v_sin_f32_e32 v16, v17
	v_cos_f32_e32 v17, v17
	s_nop 0
	v_pk_mul_f32 v[24:25], v[16:17], v[20:21]
	s_nop 0
	v_add_f32_e32 v28, v24, v25
	v_mov_b32_e32 v24, v17
	v_mov_b32_e32 v25, v16
	v_pk_mul_f32 v[16:17], v[24:25], v[20:21]
	v_and_b32_e32 v21, 0xffff0000, v18
	v_sub_f32_e32 v16, v16, v17
	v_cndmask_b32_e64 v20, v28, v16, s[40:41]
	v_exp_f32_e32 v16, 0xc0acbd82
	v_mul_f32_e32 v195, 0x3dd53b94, v20
	v_and_b32_e32 v20, 0xffff0000, v22
	v_mul_f32_e32 v16, v16, v34
	v_mul_f32_e32 v17, 0.15915494, v16
	v_floor_f32_e32 v17, v17
	v_fma_f32 v17, v16, 0.15915494, -v17
	v_sin_f32_e32 v16, v17
	v_cos_f32_e32 v17, v17
	s_nop 0
	v_pk_mul_f32 v[24:25], v[16:17], v[20:21]
	s_nop 0
	v_add_f32_e32 v18, v24, v25
	v_mov_b32_e32 v24, v17
	v_mov_b32_e32 v25, v16
	v_pk_mul_f32 v[16:17], v[24:25], v[20:21]
	v_lshlrev_b32_e32 v21, 16, v19
	v_sub_f32_e32 v16, v16, v17
	v_cndmask_b32_e64 v18, v18, v16, s[40:41]
	v_exp_f32_e32 v16, 0xc0ba0729
	v_lshlrev_b32_e32 v20, 16, v23
	v_mul_f32_e32 v22, 0x3dd53b94, v18
	v_and_b32_e32 v19, 0xffff0000, v19
	v_mul_f32_e32 v16, v16, v34
	v_mul_f32_e32 v17, 0.15915494, v16
	v_floor_f32_e32 v17, v17
	v_fma_f32 v17, v16, 0.15915494, -v17
	v_sin_f32_e32 v16, v17
	v_cos_f32_e32 v17, v17
	v_cvt_pk_fp8_f32 v195, v195, v22
	v_pk_mul_f32 v[24:25], v[16:17], v[20:21]
	s_nop 0
	v_add_f32_e32 v18, v24, v25
	v_mov_b32_e32 v24, v17
	v_mov_b32_e32 v25, v16
	v_pk_mul_f32 v[16:17], v[24:25], v[20:21]
	s_nop 0
	v_sub_f32_e32 v16, v16, v17
	v_cndmask_b32_e64 v18, v18, v16, s[40:41]
	v_exp_f32_e32 v16, 0xc0c750d0
	v_mul_f32_e32 v24, 0x3dd53b94, v18
	v_and_b32_e32 v18, 0xffff0000, v23
	v_mul_f32_e32 v16, v16, v34
	v_mul_f32_e32 v17, 0.15915494, v16
	v_floor_f32_e32 v17, v17
	v_fma_f32 v17, v16, 0.15915494, -v17
	v_sin_f32_e32 v16, v17
	v_cos_f32_e32 v17, v17
	s_nop 0
	v_pk_mul_f32 v[20:21], v[16:17], v[18:19]
	s_nop 0
	v_add_f32_e32 v23, v20, v21
	v_mov_b32_e32 v20, v17
	v_mov_b32_e32 v21, v16
	v_pk_mul_f32 v[16:17], v[20:21], v[18:19]
	s_waitcnt vmcnt(0)
	v_lshlrev_b32_e32 v19, 16, v12
	v_sub_f32_e32 v16, v16, v17
	v_cndmask_b32_e64 v16, v23, v16, s[40:41]
	v_mul_f32_e32 v18, 0x3dd53b94, v16
	v_exp_f32_e32 v16, 0xc0d49a78
	v_cvt_pk_fp8_f32 v195, v24, v18 op_sel:[0,0,1]
	v_lshlrev_b32_e32 v18, 16, v8
	v_mul_f32_e32 v16, v16, v34
	v_mul_f32_e32 v17, 0.15915494, v16
	v_floor_f32_e32 v17, v17
	v_fma_f32 v17, v16, 0.15915494, -v17
	v_sin_f32_e32 v16, v17
	v_cos_f32_e32 v17, v17
	s_nop 0
	v_pk_mul_f32 v[20:21], v[16:17], v[18:19]
	s_nop 0
	v_add_f32_e32 v22, v20, v21
	v_mov_b32_e32 v20, v17
	v_mov_b32_e32 v21, v16
	v_pk_mul_f32 v[16:17], v[20:21], v[18:19]
	v_and_b32_e32 v19, 0xffff0000, v12
	v_sub_f32_e32 v16, v16, v17
	v_cndmask_b32_e64 v18, v22, v16, s[40:41]
	v_exp_f32_e32 v16, 0xc0e1e420
	v_mul_f32_e32 v196, 0x3dd53b94, v18
	v_and_b32_e32 v18, 0xffff0000, v8
	v_mul_f32_e32 v16, v16, v34
	v_mul_f32_e32 v17, 0.15915494, v16
	v_floor_f32_e32 v17, v17
	v_fma_f32 v17, v16, 0.15915494, -v17
	v_sin_f32_e32 v16, v17
	v_cos_f32_e32 v17, v17
	s_nop 0
	v_pk_mul_f32 v[20:21], v[16:17], v[18:19]
	s_nop 0
	v_add_f32_e32 v8, v20, v21
	v_mov_b32_e32 v20, v17
	v_mov_b32_e32 v21, v16
	v_pk_mul_f32 v[16:17], v[20:21], v[18:19]
	v_lshlrev_b32_e32 v19, 16, v13
	v_sub_f32_e32 v12, v16, v17
	v_cndmask_b32_e64 v8, v8, v12, s[40:41]
	v_exp_f32_e32 v12, 0xc0ef2dc7
	v_lshlrev_b32_e32 v18, 16, v9
	v_mul_f32_e32 v22, 0x3dd53b94, v8
	v_and_b32_e32 v13, 0xffff0000, v13
	v_mul_f32_e32 v12, v12, v34
	v_mul_f32_e32 v16, 0.15915494, v12
	v_floor_f32_e32 v16, v16
	v_fma_f32 v12, v12, 0.15915494, -v16
	v_sin_f32_e32 v16, v12
	v_cos_f32_e32 v17, v12
	v_cvt_pk_fp8_f32 v196, v196, v22
	v_pk_mul_f32 v[20:21], v[16:17], v[18:19]
	s_nop 0
; __device__ __forceinline__ float bflo(unsigned w) { return __uint_as_float(w << 16); }
; __device__ __forceinline__ float bfhi(unsigned w) { return __uint_as_float(w & 0xffff0000u); }
; __device__ __forceinline__ float inv_freq32(int i) { return __builtin_amdgcn_exp2f(-(float)i * 0.41524101186092029f); }
; template <int NKS, bool MACC>
; __device__ __forceinline__ void attn_dense8_dma(int wv, const D8Args a, LAS unsigned char* ldsl) {
;     ...
;           for (int c = 0; c < 4; ++c) { const u32x4 v1 = *(const u32x4*)(qp + 8 * c), v2 = *(const u32x4*)(qp + 32 + 8 * c);
;               const unsigned a1[4] = {v1.x, v1.y, v1.z, v1.w}, a2[4] = {v2.x, v2.y, v2.z, v2.w}; float y[8];
; #pragma unroll
;               for (int e = 0; e < 8; ++e) { const int i = 8 * c + e; float sn, cs; sincos_rev(pos * inv_freq32(i), sn, cs);
;                   const float x1 = (e & 1) ? bfhi(a1[e >> 1]) : bflo(a1[e >> 1]), x2 = (e & 1) ? bfhi(a2[e >> 1]) : bflo(a2[e >> 1]);
;                   y[e] = (hi ? (x2 * cs + x1 * sn) : (x1 * cs - x2 * sn)) * QC; }
;               w[2 * c] = pk4_fp8(y[0], y[1], y[2], y[3]); w[2 * c + 1] = pk4_fp8(y[4], y[5], y[6], y[7]); }
	v_add_f32_e32 v8, v20, v21
	v_mov_b32_e32 v20, v17
	v_mov_b32_e32 v21, v16
	v_pk_mul_f32 v[16:17], v[20:21], v[18:19]
	s_nop 0
	v_sub_f32_e32 v12, v16, v17
	v_cndmask_b32_e64 v8, v8, v12, s[40:41]
	v_exp_f32_e32 v12, 0xc0fc776e
	v_mul_f32_e32 v18, 0x3dd53b94, v8
	v_mul_f32_e32 v12, v12, v34
	v_mul_f32_e32 v16, 0.15915494, v12
	v_floor_f32_e32 v16, v16
	v_fma_f32 v12, v12, 0.15915494, -v16
	v_sin_f32_e32 v16, v12
	v_cos_f32_e32 v17, v12
	v_and_b32_e32 v12, 0xffff0000, v9
	v_pk_mul_f32 v[8:9], v[16:17], v[12:13]
	s_nop 0
	v_add_f32_e32 v19, v8, v9
	v_mov_b32_e32 v8, v17
	v_mov_b32_e32 v9, v16
	v_pk_mul_f32 v[8:9], v[8:9], v[12:13]
	v_lshlrev_b32_e32 v13, 16, v14
	v_sub_f32_e32 v8, v8, v9
	v_cndmask_b32_e64 v12, v19, v8, s[40:41]
	v_exp_f32_e32 v8, 0xc104e08b
	v_mul_f32_e32 v19, 0x3dd53b94, v12
	v_lshlrev_b32_e32 v12, 16, v10
	v_cvt_pk_fp8_f32 v196, v18, v19 op_sel:[0,0,1]
	v_mul_f32_e32 v8, v8, v34
	v_mul_f32_e32 v9, 0.15915494, v8
	v_floor_f32_e32 v9, v9
	v_fma_f32 v9, v8, 0.15915494, -v9
	v_sin_f32_e32 v8, v9
	v_cos_f32_e32 v9, v9
	s_nop 0
	v_pk_mul_f32 v[16:17], v[8:9], v[12:13]
	s_nop 0
	v_add_f32_e32 v20, v16, v17
	v_mov_b32_e32 v16, v9
	v_mov_b32_e32 v17, v8
	v_pk_mul_f32 v[8:9], v[16:17], v[12:13]
	v_and_b32_e32 v13, 0xffff0000, v14
	v_sub_f32_e32 v8, v8, v9
	v_cndmask_b32_e64 v12, v20, v8, s[40:41]
	v_exp_f32_e32 v8, 0xc10b855f
	v_mul_f32_e32 v197, 0x3dd53b94, v12
	v_and_b32_e32 v12, 0xffff0000, v10
	v_mul_f32_e32 v8, v8, v34
	v_mul_f32_e32 v9, 0.15915494, v8
	v_floor_f32_e32 v9, v9
	v_fma_f32 v9, v8, 0.15915494, -v9
	v_sin_f32_e32 v8, v9
	v_cos_f32_e32 v9, v9
	s_nop 0
	v_pk_mul_f32 v[16:17], v[8:9], v[12:13]
	s_nop 0
	v_add_f32_e32 v10, v16, v17
	v_mov_b32_e32 v16, v9
	v_mov_b32_e32 v17, v8
	v_pk_mul_f32 v[8:9], v[16:17], v[12:13]
	v_lshlrev_b32_e32 v13, 16, v15
	v_sub_f32_e32 v8, v8, v9
	v_cndmask_b32_e64 v10, v10, v8, s[40:41]
	v_exp_f32_e32 v8, 0xc1122a32
	v_lshlrev_b32_e32 v12, 16, v11
	v_mul_f32_e32 v14, 0x3dd53b94, v10
	v_cvt_pk_fp8_f32 v197, v197, v14
	v_mul_f32_e32 v8, v8, v34
	v_mul_f32_e32 v9, 0.15915494, v8
	v_floor_f32_e32 v9, v9
	v_fma_f32 v9, v8, 0.15915494, -v9
	v_sin_f32_e32 v8, v9
	v_cos_f32_e32 v9, v9
	s_nop 0
	v_pk_mul_f32 v[16:17], v[8:9], v[12:13]
	s_nop 0
	v_add_f32_e32 v10, v16, v17
	v_mov_b32_e32 v16, v9
	v_mov_b32_e32 v17, v8
	v_pk_mul_f32 v[8:9], v[16:17], v[12:13]
	v_and_b32_e32 v13, 0xffff0000, v15
	v_sub_f32_e32 v8, v8, v9
	v_cndmask_b32_e64 v10, v10, v8, s[40:41]
	v_exp_f32_e32 v8, 0xc118cf06
	v_and_b32_e32 v12, 0xffff0000, v11
	v_mul_f32_e32 v16, 0x3dd53b94, v10
	v_mul_f32_e32 v8, v8, v34
	v_mul_f32_e32 v9, 0.15915494, v8
	v_floor_f32_e32 v9, v9
	v_fma_f32 v9, v8, 0.15915494, -v9
	v_sin_f32_e32 v8, v9
	v_cos_f32_e32 v9, v9
	s_nop 0
	v_pk_mul_f32 v[10:11], v[8:9], v[12:13]
	s_nop 0
	v_add_f32_e32 v15, v10, v11
	v_mov_b32_e32 v10, v9
	v_mov_b32_e32 v11, v8
	v_pk_mul_f32 v[8:9], v[10:11], v[12:13]
	v_lshlrev_b32_e32 v11, 16, v4
	v_sub_f32_e32 v8, v8, v9
	v_cndmask_b32_e64 v8, v15, v8, s[40:41]
	v_mul_f32_e32 v10, 0x3dd53b94, v8
	v_exp_f32_e32 v8, 0xc11f73da
	v_cvt_pk_fp8_f32 v197, v16, v10 op_sel:[0,0,1]
	v_lshlrev_b32_e32 v10, 16, v0
	v_mul_f32_e32 v8, v8, v34
	v_mul_f32_e32 v9, 0.15915494, v8
	v_floor_f32_e32 v9, v9
	v_fma_f32 v9, v8, 0.15915494, -v9
	v_sin_f32_e32 v8, v9
	v_cos_f32_e32 v9, v9
	s_nop 0
	v_pk_mul_f32 v[12:13], v[8:9], v[10:11]
	s_nop 0
	v_add_f32_e32 v14, v12, v13
	v_mov_b32_e32 v12, v9
	v_mov_b32_e32 v13, v8
	v_pk_mul_f32 v[8:9], v[12:13], v[10:11]
	v_and_b32_e32 v11, 0xffff0000, v4
	v_sub_f32_e32 v8, v8, v9
	v_cndmask_b32_e64 v10, v14, v8, s[40:41]
	v_exp_f32_e32 v8, 0xc12618ae
	v_mul_f32_e32 v198, 0x3dd53b94, v10
	v_and_b32_e32 v10, 0xffff0000, v0
	v_mul_f32_e32 v8, v8, v34
	v_mul_f32_e32 v9, 0.15915494, v8
	v_floor_f32_e32 v9, v9
	v_fma_f32 v9, v8, 0.15915494, -v9
	v_sin_f32_e32 v8, v9
	v_cos_f32_e32 v9, v9
	s_nop 0
	v_pk_mul_f32 v[12:13], v[8:9], v[10:11]
	s_nop 0
	v_add_f32_e32 v0, v12, v13
	v_mov_b32_e32 v12, v9
	v_mov_b32_e32 v13, v8
	v_pk_mul_f32 v[8:9], v[12:13], v[10:11]
	v_lshlrev_b32_e32 v11, 16, v5
	v_sub_f32_e32 v4, v8, v9
	v_cndmask_b32_e64 v0, v0, v4, s[40:41]
	v_exp_f32_e32 v4, 0xc12cbd82
	v_lshlrev_b32_e32 v10, 16, v1
	v_mul_f32_e32 v14, 0x3dd53b94, v0
	v_and_b32_e32 v5, 0xffff0000, v5
	v_mul_f32_e32 v4, v4, v34
	v_mul_f32_e32 v8, 0.15915494, v4
	v_floor_f32_e32 v8, v8
	v_fma_f32 v4, v4, 0.15915494, -v8
	v_sin_f32_e32 v8, v4
	v_cos_f32_e32 v9, v4
	v_cvt_pk_fp8_f32 v198, v198, v14
	v_pk_mul_f32 v[12:13], v[8:9], v[10:11]
	s_nop 0
	v_add_f32_e32 v0, v12, v13
	v_mov_b32_e32 v12, v9
	v_mov_b32_e32 v13, v8
	v_pk_mul_f32 v[8:9], v[12:13], v[10:11]
	s_nop 0
	v_sub_f32_e32 v4, v8, v9
	v_cndmask_b32_e64 v0, v0, v4, s[40:41]
	v_exp_f32_e32 v4, 0xc1336255
	v_mul_f32_e32 v10, 0x3dd53b94, v0
	v_mul_f32_e32 v4, v4, v34
	v_mul_f32_e32 v8, 0.15915494, v4
	v_floor_f32_e32 v8, v8
	v_fma_f32 v4, v4, 0.15915494, -v8
	v_sin_f32_e32 v8, v4
	v_cos_f32_e32 v9, v4
	v_and_b32_e32 v4, 0xffff0000, v1
	v_pk_mul_f32 v[0:1], v[8:9], v[4:5]
	s_nop 0
	v_add_f32_e32 v11, v0, v1
	v_mov_b32_e32 v0, v9
	v_mov_b32_e32 v1, v8
	v_pk_mul_f32 v[0:1], v[0:1], v[4:5]
	v_lshlrev_b32_e32 v5, 16, v6
	v_sub_f32_e32 v0, v0, v1
	v_cndmask_b32_e64 v4, v11, v0, s[40:41]
	v_exp_f32_e32 v0, 0xc13a0729
	v_mul_f32_e32 v11, 0x3dd53b94, v4
	v_lshlrev_b32_e32 v4, 16, v2
	v_cvt_pk_fp8_f32 v198, v10, v11 op_sel:[0,0,1]
	v_mul_f32_e32 v0, v0, v34
	v_mul_f32_e32 v1, 0.15915494, v0
	v_floor_f32_e32 v1, v1
	v_fma_f32 v1, v0, 0.15915494, -v1
	v_sin_f32_e32 v0, v1
	v_cos_f32_e32 v1, v1
	s_nop 0
	v_pk_mul_f32 v[8:9], v[0:1], v[4:5]
	s_nop 0
	v_add_f32_e32 v12, v8, v9
	v_mov_b32_e32 v8, v1
	v_mov_b32_e32 v9, v0
	v_pk_mul_f32 v[0:1], v[8:9], v[4:5]
; #define SBAR() __builtin_amdgcn_sched_barrier(0)
; #define SBAR() __builtin_amdgcn_sched_barrier(0)
; #define RESC8(al) do { if (__any((al) < 1.f)) { if (hi == 0) al_l[r32] = (al); asm volatile("s_waitcnt lgkmcnt(0)" ::: "memory"); \
;     _Pragma("unroll") for (int d = 0; d < 4; ++d) _Pragma("unroll") for (int r = 0; r < 16; ++r) o[d][r] *= al_l[da::crow(r, hi)]; } } while (0)
; #define RESC8(al) do { if (__any((al) < 1.f)) { if (hi == 0) al_l[r32] = (al); asm volatile("s_waitcnt lgkmcnt(0)" ::: "memory"); \
;     _Pragma("unroll") for (int d = 0; d < 4; ++d) _Pragma("unroll") for (int r = 0; r < 16; ++r) o[d][r] *= al_l[da::crow(r, hi)]; \
;     if constexpr (LSUM) { _Pragma("unroll") for (int r = 0; r < 16; ++r) lacc[r] *= al_l[da::crow(r, hi)]; } } } while (0)
; #define D8Qm(P0, P1, b) qkt8d<NKS, MACC>(P0, P1, mneg, ldsl, kb0 + (b) * K8_BYTES, rb0 + (b) * KR8_BYTES, qf)
; template <bool FIRST, bool SPLAT = false>
; __device__ __forceinline__ void partialSM8(f32x16& p0, f32x16& p1, float& m_reg, f32x16& mneg, float& alpha) {
;     float pmax = p0[0];
; #pragma unroll
;     for (int r = 1; r < 16; ++r) pmax = fmaxf(pmax, p0[r]);
; #pragma unroll
;     for (int r = 0; r < 16; ++r) pmax = fmaxf(pmax, p1[r]);
;     { auto rr = __builtin_amdgcn_permlane32_swap(__float_as_uint(pmax), __float_as_uint(pmax), false, false);
;       pmax = fmaxf(__uint_as_float(rr[0]), __uint_as_float(rr[1])); }
;     if (!FIRST && __builtin_expect(__all(pmax <= THR8 * LOG2E), 1)) { alpha = 1.f; }
;     else { const float delta = FIRST ? pmax : fmaxf(pmax, 0.f); alpha = FIRST ? 1.f : __builtin_amdgcn_exp2f(-delta); m_reg += delta;
; #pragma unroll
;         for (int r = 0; r < 16; ++r) { p0[r] -= delta; p1[r] -= delta; }
;         if constexpr (!SPLAT) { const float nm = -m_reg;
; #pragma unroll
;             for (int r = 0; r < 16; ++r) mneg[r] = nm; } }
;     if constexpr (SPLAT) { float nm = -m_reg; asm volatile("" : "+v"(nm));
; #pragma unroll
;         for (int r = 0; r < 16; ++r) mneg[r] = nm; }
; #pragma unroll
;     for (int r = 0; r < 16; ++r) p0[r] = __builtin_amdgcn_exp2f(p0[r]);
; }
; template <int NKS, bool MACC>
; __device__ __forceinline__ void attn_dense8_dma(int wv, const D8Args a, LAS unsigned char* ldsl) {
;     ...
;     D8_TOP();
;     D8Qm(pA0, pA1, 0); D8Pm(true, pA0, pA1, alA); RESC8(alA);
;     SBAR(); D8Qm(pB0, pB1, 1);
	v_and_b32_e32 v5, 0xffff0000, v6
	v_sub_f32_e32 v0, v0, v1
	v_cndmask_b32_e64 v4, v12, v0, s[40:41]
	v_exp_f32_e32 v0, 0xc140abfd
	v_mul_f32_e32 v199, 0x3dd53b94, v4
	v_and_b32_e32 v4, 0xffff0000, v2
	v_mul_f32_e32 v0, v0, v34
	v_mul_f32_e32 v1, 0.15915494, v0
	v_floor_f32_e32 v1, v1
	v_fma_f32 v1, v0, 0.15915494, -v1
	v_sin_f32_e32 v0, v1
	v_cos_f32_e32 v1, v1
	s_nop 0
	v_pk_mul_f32 v[8:9], v[0:1], v[4:5]
	s_nop 0
	v_add_f32_e32 v2, v8, v9
	v_mov_b32_e32 v8, v1
	v_mov_b32_e32 v9, v0
	v_pk_mul_f32 v[0:1], v[8:9], v[4:5]
	v_lshlrev_b32_e32 v5, 16, v7
	v_sub_f32_e32 v0, v0, v1
	v_cndmask_b32_e64 v2, v2, v0, s[40:41]
	v_exp_f32_e32 v0, 0xc14750d0
	v_lshlrev_b32_e32 v4, 16, v3
	v_mul_f32_e32 v6, 0x3dd53b94, v2
	v_cvt_pk_fp8_f32 v199, v199, v6
	v_mul_f32_e32 v0, v0, v34
	v_mul_f32_e32 v1, 0.15915494, v0
	v_floor_f32_e32 v1, v1
	v_fma_f32 v1, v0, 0.15915494, -v1
	v_sin_f32_e32 v0, v1
	v_cos_f32_e32 v1, v1
	s_nop 0
	v_pk_mul_f32 v[8:9], v[0:1], v[4:5]
	s_nop 0
	v_add_f32_e32 v2, v8, v9
	v_mov_b32_e32 v8, v1
	v_mov_b32_e32 v9, v0
	v_pk_mul_f32 v[0:1], v[8:9], v[4:5]
	v_and_b32_e32 v5, 0xffff0000, v7
	v_sub_f32_e32 v0, v0, v1
	v_cndmask_b32_e64 v2, v2, v0, s[40:41]
	v_exp_f32_e32 v0, 0xc14df5a4
	v_and_b32_e32 v4, 0xffff0000, v3
	v_mul_f32_e32 v8, 0x3dd53b94, v2
	v_mul_f32_e32 v0, v0, v34
	v_mul_f32_e32 v1, 0.15915494, v0
	v_floor_f32_e32 v1, v1
	v_fma_f32 v1, v0, 0.15915494, -v1
	v_sin_f32_e32 v0, v1
	v_cos_f32_e32 v1, v1
	s_nop 0
	v_pk_mul_f32 v[2:3], v[0:1], v[4:5]
	s_nop 0
	v_add_f32_e32 v7, v2, v3
	v_mov_b32_e32 v2, v1
	v_mov_b32_e32 v3, v0
	v_pk_mul_f32 v[0:1], v[2:3], v[4:5]
	s_nop 0
	v_sub_f32_e32 v0, v0, v1
	v_cndmask_b32_e64 v0, v7, v0, s[40:41]
	v_mul_f32_e32 v0, 0x3dd53b94, v0
	v_cvt_pk_fp8_f32 v199, v8, v0 op_sel:[0,0,1]
	v_lshlrev_b32_e32 v1, 3, v32
	v_lshlrev_b32_e32 v0, 7, v72
	v_and_b32_e32 v2, 0x70, v1
	v_bitop3_b32 v1, v1, v33, s89 bitop3:0x6c
	v_bitop3_b32 v202, v2, v0, v33 bitop3:0xde
	s_movk_i32 s0, 0x50
	v_add_u32_e32 v59, 0, v202
	v_xad_u32 v61, v202, 64, 0
	v_bitop3_b32 v0, v1, s0, v0 bitop3:0x36
	s_waitcnt vmcnt(0)
	s_waitcnt lgkmcnt(0)
	s_barrier
	v_xad_u32 v60, v202, 16, 0
	ds_read_b128 v[16:19], v59
	ds_read_b128 v[50:53], v59 offset:4096
	ds_read_b128 v[20:23], v60
	ds_read_b128 v[54:57], v60 offset:4096
	v_add_u32_e32 v62, 0, v0
	ds_read_b128 v[24:27], v61
	ds_read_b128 v[74:77], v61 offset:4096
	ds_read_b128 v[28:31], v62
	ds_read_b128 v[78:81], v62 offset:4096
	v_lshlrev_b32_e32 v2, 2, v32
	v_lshlrev_b32_e32 v49, 6, v72
	v_and_b32_e32 v3, 48, v2
	s_waitcnt lgkmcnt(0)
	v_bitop3_b32 v200, v3, v49, v33 bitop3:0xde
	v_or_b32_e32 v203, 0x12000, v200
	v_bitop3_b32 v58, v2, v33, 48 bitop3:0x6c
	v_readlane_b32 s76, v254, 31
	v_readlane_b32 s77, v254, 32
	v_readlane_b32 s78, v254, 33
	v_readlane_b32 s79, v254, 34
	v_readlane_b32 s80, v254, 35
	v_readlane_b32 s81, v254, 36
	v_readlane_b32 s82, v254, 37
	v_readlane_b32 s83, v254, 38
	v_readlane_b32 s84, v254, 39
	v_readlane_b32 s85, v254, 40
	v_readlane_b32 s86, v254, 41
	v_readlane_b32 s87, v254, 42
	v_readlane_b32 s88, v254, 43
	v_readlane_b32 s89, v254, 44
	v_readlane_b32 s90, v254, 45
	v_readlane_b32 s91, v254, 46
	v_mov_b64_e32 v[32:33], s[76:77]
	v_mov_b64_e32 v[34:35], s[78:79]
	v_mov_b64_e32 v[36:37], s[80:81]
	v_mov_b64_e32 v[38:39], s[82:83]
	v_mov_b64_e32 v[40:41], s[84:85]
	v_mov_b64_e32 v[42:43], s[86:87]
	v_mov_b64_e32 v[44:45], s[88:89]
	v_mov_b64_e32 v[46:47], s[90:91]
	s_waitcnt lgkmcnt(5)
	v_mfma_f32_32x32x64_f8f6f4 v[0:15], v[16:23], v[176:183], v[32:47]
	v_xad_u32 v63, v200, 16, 0
	s_waitcnt lgkmcnt(1)
	v_mfma_f32_32x32x64_f8f6f4 v[0:15], v[24:31], v[184:191], v[0:15]
	v_mfma_f32_32x32x64_f8f6f4 v[16:31], v[50:57], v[176:183], v[32:47]
	v_add_u32_e32 v201, 0, v200
	ds_read_b128 v[54:57], v63 offset:49152
	ds_read_b128 v[50:53], v201 offset:49152
	s_waitcnt lgkmcnt(2)
	v_mfma_f32_32x32x64_f8f6f4 v[16:31], v[74:81], v[184:191], v[16:31]
	s_waitcnt lgkmcnt(0)
	v_mfma_f32_32x32x64_f8f6f4 v[0:15], v[50:57], v[192:199], v[0:15]
	ds_read_b128 v[50:53], v201 offset:51200
	ds_read_b128 v[54:57], v63 offset:51200
	s_waitcnt lgkmcnt(0)
	v_mfma_f32_32x32x64_f8f6f4 v[16:31], v[50:57], v[192:199], v[16:31]
	s_nop 15
	v_max_f32_e32 v32, v1, v1
	v_max_f32_e32 v33, v0, v0
	v_max_f32_e32 v32, v33, v32
	v_max3_f32 v32, v32, v2, v3
	v_max3_f32 v32, v32, v4, v5
	v_max3_f32 v32, v32, v6, v7
	v_max3_f32 v32, v32, v8, v9
	v_max3_f32 v32, v32, v10, v11
	v_max3_f32 v32, v32, v12, v13
	v_max3_f32 v32, v32, v14, v15
	v_max3_f32 v32, v32, v16, v17
	v_max3_f32 v32, v32, v18, v19
	v_max3_f32 v32, v32, v20, v21
	v_max3_f32 v32, v32, v22, v23
	v_max3_f32 v32, v32, v24, v25
	v_max3_f32 v32, v32, v26, v27
	v_max3_f32 v32, v32, v28, v29
	v_max3_f32 v32, v32, v30, v31
	v_mov_b32_e32 v33, v32
	s_nop 1
	v_permlane32_swap_b32_e32 v32, v33
	v_max_f32_e32 v33, v33, v33
	v_max_f32_e32 v32, v32, v32
	v_max_f32_e32 v32, v32, v33
	v_sub_f32_e32 v1, v1, v32
	v_sub_f32_e32 v2, v2, v32
	v_sub_f32_e32 v3, v3, v32
	v_sub_f32_e32 v5, v5, v32
	v_sub_f32_e32 v6, v6, v32
	v_sub_f32_e32 v7, v7, v32
	v_sub_f32_e32 v9, v9, v32
	v_sub_f32_e32 v10, v10, v32
	v_sub_f32_e32 v11, v11, v32
	v_sub_f32_e32 v13, v13, v32
	v_sub_f32_e32 v14, v14, v32
	v_sub_f32_e32 v15, v15, v32
	v_exp_f32_e32 v117, v1
	v_exp_f32_e32 v118, v2
	v_exp_f32_e32 v119, v3
	v_exp_f32_e32 v120, v5
	v_exp_f32_e32 v121, v6
	v_exp_f32_e32 v122, v7
	v_exp_f32_e32 v123, v9
	v_exp_f32_e32 v124, v10
	v_exp_f32_e32 v125, v11
	v_exp_f32_e32 v126, v13
	v_exp_f32_e32 v127, v14
	v_exp_f32_e32 v128, v15
	v_add_f32_e32 v204, 0, v32
	v_sub_f32_e32 v0, v0, v32
	v_xor_b32_e32 v64, 0x80000000, v204
	v_sub_f32_e32 v44, v16, v32
	v_sub_f32_e32 v4, v4, v32
	v_sub_f32_e32 v73, v20, v32
	v_sub_f32_e32 v74, v21, v32
	v_sub_f32_e32 v8, v8, v32
	v_sub_f32_e32 v112, v27, v32
	v_sub_f32_e32 v12, v12, v32
	v_sub_f32_e32 v113, v28, v32
	v_sub_f32_e32 v114, v29, v32
	v_sub_f32_e32 v115, v30, v32
	v_sub_f32_e32 v116, v31, v32
	v_exp_f32_e32 v16, v0
	v_mov_b32_e32 v0, v64
	v_sub_f32_e32 v45, v17, v32
	v_sub_f32_e32 v46, v18, v32
	v_sub_f32_e32 v47, v19, v32
	v_sub_f32_e32 v75, v22, v32
	v_sub_f32_e32 v76, v23, v32
	v_sub_f32_e32 v77, v24, v32
	v_sub_f32_e32 v78, v25, v32
	v_sub_f32_e32 v79, v26, v32
	v_exp_f32_e32 v17, v4
	v_exp_f32_e32 v18, v8
	v_exp_f32_e32 v19, v12
	ds_read_b128 v[20:23], v59 offset:8192
	ds_read_b128 v[28:31], v59 offset:12288
	ds_read_b128 v[24:27], v60 offset:8192
	ds_read_b128 v[32:35], v60 offset:12288
	ds_read_b128 v[36:39], v61 offset:8192
	ds_read_b128 v[50:53], v61 offset:12288
	ds_read_b128 v[40:43], v62 offset:8192
	ds_read_b128 v[54:57], v62 offset:12288
	s_waitcnt lgkmcnt(0)
; #define SBAR() __builtin_amdgcn_sched_barrier(0)
; #define SBAR() __builtin_amdgcn_sched_barrier(0)
; #define D8Qm(P0, P1, b) qkt8d<NKS, MACC>(P0, P1, mneg, ldsl, kb0 + (b) * K8_BYTES, rb0 + (b) * KR8_BYTES, qf)
; #define D8Vm(b) do { pv8d(o, ldsl, vb0 + (b) * K8_BYTES, pa); if constexpr (LSUM) lacc = D8_MX(pa, ones8, lacc); } while (0)
; #define D8Fm(P0, P1, AL) do { if constexpr (LSUM) finishSM8n(P0, P1, pa); else finishSM8(P0, P1, AL, l_reg, pa); } while (0)
; #define D8Pm(FIRST, P0, P1, AL) do { if constexpr (MACC) partialSM8<FIRST, (NKS == 3)>(P0, P1, m_reg, mneg, AL); else partialSM8z<NKS>(P0, P1, m_reg, AL); } while (0)
; __device__ __forceinline__ void finishSM8(f32x16& p0, f32x16& p1, float alpha, float& l_reg, i32x8& pa) {
; #pragma unroll
;     for (int r = 0; r < 16; ++r) p1[r] = __builtin_amdgcn_exp2f(p1[r]);
;     float ps = 0;
; #pragma unroll
;     for (int r = 0; r < 16; ++r) ps += p0[r];
; #pragma unroll
;     for (int r = 0; r < 16; ++r) ps += p1[r];
;     { auto rr = __builtin_amdgcn_permlane32_swap(__float_as_uint(ps), __float_as_uint(ps), false, false);
;       ps = __uint_as_float(rr[0]) + __uint_as_float(rr[1]); }
;     l_reg = l_reg * alpha + ps;
;     pa = (i32x8){(int)pk4_fp8(p0[0], p0[1], p0[2], p0[3]), (int)pk4_fp8(p0[4], p0[5], p0[6], p0[7]), (int)pk4_fp8(p0[8], p0[9], p0[10], p0[11]), (int)pk4_fp8(p0[12], p0[13], p0[14], p0[15]),
;                  (int)pk4_fp8(p1[0], p1[1], p1[2], p1[3]), (int)pk4_fp8(p1[4], p1[5], p1[6], p1[7]), (int)pk4_fp8(p1[8], p1[9], p1[10], p1[11]), (int)pk4_fp8(p1[12], p1[13], p1[14], p1[15])};
; }
; template <int NKS, bool MACC>
; __device__ __forceinline__ void attn_dense8_dma(int wv, const D8Args a, LAS unsigned char* ldsl) {
;     ...
;     SBAR(); D8Qm(pB0, pB1, 1);
;     D8Fm(pA0, pA1, alA); SBAR();
;     D8Vm(0); D8Pm(false, pB0, pB1, alB);
	v_mov_b32_e32 v1, v0
	v_mov_b32_e32 v2, v0
	v_mov_b32_e32 v3, v0
	v_mov_b32_e32 v4, v0
	v_mov_b32_e32 v5, v0
	v_mov_b32_e32 v6, v0
	v_mov_b32_e32 v7, v0
	v_mov_b32_e32 v8, v0
	v_mov_b32_e32 v9, v0
	v_mov_b32_e32 v10, v0
	v_mov_b32_e32 v11, v0
	v_mov_b32_e32 v12, v0
	v_mov_b32_e32 v13, v0
	v_mov_b32_e32 v14, v0
	v_mov_b32_e32 v15, v0
	s_waitcnt lgkmcnt(5)
	v_mfma_f32_32x32x64_f8f6f4 v[96:111], v[20:27], v[176:183], v[0:15]
	s_waitcnt lgkmcnt(4)
	v_mfma_f32_32x32x64_f8f6f4 v[80:95], v[28:35], v[176:183], v[0:15]
	ds_read_b128 v[24:27], v63 offset:53248
	ds_read_b128 v[20:23], v201 offset:53248
	ds_read_b128 v[28:31], v201 offset:55296
	ds_read_b128 v[32:35], v63 offset:55296
	s_waitcnt lgkmcnt(5)
	v_mfma_f32_32x32x64_f8f6f4 v[96:111], v[36:43], v[184:191], v[96:111]
	s_waitcnt lgkmcnt(4)
	v_mfma_f32_32x32x64_f8f6f4 v[80:95], v[50:57], v[184:191], v[80:95]
	s_waitcnt lgkmcnt(2)
	v_mfma_f32_32x32x64_f8f6f4 v[96:111], v[20:27], v[192:199], v[96:111]
	v_exp_f32_e32 v20, v44
	v_exp_f32_e32 v21, v73
	v_exp_f32_e32 v22, v77
	v_exp_f32_e32 v23, v113
	s_waitcnt lgkmcnt(0)
	v_mfma_f32_32x32x64_f8f6f4 v[80:95], v[28:35], v[192:199], v[80:95]
	v_add_f32_e32 v12, 0, v16
	v_add_f32_e32 v12, v117, v12
	v_add_f32_e32 v12, v118, v12
	v_add_f32_e32 v12, v119, v12
	v_add_f32_e32 v12, v17, v12
	v_add_f32_e32 v12, v120, v12
	v_add_f32_e32 v12, v121, v12
	v_add_f32_e32 v12, v122, v12
	v_add_f32_e32 v12, v18, v12
	v_add_f32_e32 v12, v123, v12
	v_add_f32_e32 v12, v124, v12
	v_add_f32_e32 v12, v125, v12
	v_add_f32_e32 v12, v19, v12
	v_exp_f32_e32 v0, v45
	v_add_f32_e32 v12, v126, v12
	v_exp_f32_e32 v1, v46
	v_add_f32_e32 v12, v127, v12
	v_exp_f32_e32 v2, v47
	v_add_f32_e32 v12, v128, v12
	v_add_f32_e32 v12, v20, v12
	v_exp_f32_e32 v3, v74
	v_add_f32_e32 v12, v0, v12
	v_exp_f32_e32 v4, v75
	v_add_f32_e32 v12, v1, v12
	v_exp_f32_e32 v5, v76
	v_add_f32_e32 v12, v2, v12
	v_add_f32_e32 v12, v21, v12
	v_exp_f32_e32 v6, v78
	v_add_f32_e32 v12, v3, v12
	v_exp_f32_e32 v7, v79
	v_add_f32_e32 v12, v4, v12
	v_exp_f32_e32 v8, v112
	v_add_f32_e32 v12, v5, v12
	v_add_f32_e32 v12, v22, v12
	v_exp_f32_e32 v9, v114
	v_add_f32_e32 v12, v6, v12
	v_exp_f32_e32 v10, v115
	v_add_f32_e32 v12, v7, v12
	v_exp_f32_e32 v11, v116
	v_add_f32_e32 v12, v8, v12
	v_add_f32_e32 v12, v23, v12
	v_add_f32_e32 v12, v9, v12
	v_add_f32_e32 v12, v10, v12
	v_cvt_pk_fp8_f32 v16, v16, v117
	v_cvt_pk_fp8_f32 v17, v17, v120
	v_cvt_pk_fp8_f32 v18, v18, v123
	v_cvt_pk_fp8_f32 v19, v19, v126
	v_cvt_pk_fp8_f32 v20, v20, v0
	v_cvt_pk_fp8_f32 v21, v21, v3
	v_cvt_pk_fp8_f32 v22, v22, v6
	v_cvt_pk_fp8_f32 v23, v23, v9
	v_add_f32_e32 v73, v11, v12
	v_mov_b32_e32 v74, v73
	s_nop 1
	v_permlane32_swap_b32_e32 v73, v74
	v_cvt_pk_fp8_f32 v16, v118, v119 op_sel:[0,0,1]
	v_cvt_pk_fp8_f32 v17, v121, v122 op_sel:[0,0,1]
	v_cvt_pk_fp8_f32 v18, v124, v125 op_sel:[0,0,1]
	v_cvt_pk_fp8_f32 v19, v127, v128 op_sel:[0,0,1]
	v_cvt_pk_fp8_f32 v20, v1, v2 op_sel:[0,0,1]
	v_cvt_pk_fp8_f32 v21, v4, v5 op_sel:[0,0,1]
	v_cvt_pk_fp8_f32 v22, v7, v8 op_sel:[0,0,1]
	v_cvt_pk_fp8_f32 v23, v10, v11 op_sel:[0,0,1]
	s_mov_b32 s0, 0x12010
	v_bitop3_b32 v0, v58, s0, v49 bitop3:0x36
	v_add_u32_e32 v205, 0, v203
	v_add_u32_e32 v36, 0, v0
	ds_read_b128 v[0:3], v205
	ds_read_b128 v[8:11], v205 offset:2048
	ds_read_b128 v[4:7], v36
	ds_read_b128 v[12:15], v36 offset:2048
	ds_read_b128 v[24:27], v205 offset:4096
	ds_read_b128 v[32:35], v205 offset:6144
	ds_read_b128 v[28:31], v36 offset:4096
	ds_read_b128 v[36:39], v36 offset:6144
	s_waitcnt lgkmcnt(0)
	s_waitcnt lgkmcnt(5)
	v_mfma_f32_32x32x64_f8f6f4 v[112:127], v[16:23], v[0:7], 0
	v_max_f32_e32 v0, v97, v97
	v_max_f32_e32 v1, v96, v96
	v_max_f32_e32 v0, v1, v0
	v_max3_f32 v0, v0, v98, v99
	v_max3_f32 v0, v0, v100, v101
	v_max3_f32 v0, v0, v102, v103
	v_max3_f32 v0, v0, v104, v105
	v_max3_f32 v0, v0, v106, v107
	v_max3_f32 v0, v0, v108, v109
	v_max3_f32 v0, v0, v110, v111
	v_max3_f32 v0, v0, v80, v81
	v_max3_f32 v0, v0, v82, v83
	v_max3_f32 v0, v0, v84, v85
	v_max3_f32 v0, v0, v86, v87
	v_max3_f32 v0, v0, v88, v89
	s_waitcnt lgkmcnt(4)
	v_mfma_f32_32x32x64_f8f6f4 v[128:143], v[16:23], v[8:15], 0
	v_max3_f32 v0, v0, v90, v91
	v_max3_f32 v0, v0, v92, v93
	v_max3_f32 v0, v0, v94, v95
	v_mov_b32_e32 v1, v0
	s_nop 1
	v_permlane32_swap_b32_e32 v0, v1
	v_max_f32_e32 v1, v1, v1
	v_max_f32_e32 v0, v0, v0
	v_max_f32_e32 v0, v0, v1
	v_cmp_ge_f32_e32 vcc, s10, v0
	s_cmp_eq_u64 vcc, exec
	s_waitcnt lgkmcnt(1)
	v_mfma_f32_32x32x64_f8f6f4 v[144:159], v[16:23], v[24:31], 0
	s_waitcnt lgkmcnt(0)
	v_mfma_f32_32x32x64_f8f6f4 v[160:175], v[16:23], v[32:39], 0
	s_cbranch_scc0 .LBB0_482
	v_mov_b32_e32 v206, 1.0

; #define SBAR() __builtin_amdgcn_sched_barrier(0)
; template <int NKS, bool MACC>
; __device__ __forceinline__ void attn_dense8_dma(int wv, const D8Args a, LAS unsigned char* ldsl) {
;     ...
;     const unsigned char* ksrc; const unsigned char* vsrc; const unsigned char* rsrc = nullptr;
;     { const int ri = 8 * wid + (lane >> 3), hk = (ri >> 2) & 1, ka = 32 * hk + (ri & 3) + 4 * ((ri >> 3) & 3) + 16 * (ri >> 5), kch = ((lane & 7) ^ (ri >> 1)) & 7;
;       ksrc = a.K8 + (long)ka * a.ldk + kch * 16;
;       const int vc = 16 * wid + (lane >> 2), vp = ((lane & 3) ^ (vc >> 2)) & 3; vsrc = a.Vt8 + (long)vc * a.ldvt + vp * 16;
;       if constexpr (NKS == 3) { const int rr = 16 * (wid & 3) + (lane >> 2), rh = (rr >> 2) & 1, ra = 32 * rh + (rr & 3) + 4 * ((rr >> 3) & 3) + 16 * (rr >> 5), rch = ((lane & 3) ^ (rr >> 2)) & 3;
;           rsrc = a.Kr8 + (long)ra * 64 + rch * 16; } }
;     ...
;     D8_DMA2(0, 0); D8_DMA2(128, 1); SBAR();
;     { const bf16_t* Qw = a.Q + (long)(wid * 32 + r32) * a.ldq;
; #pragma unroll
;       for (int sK = 0; sK < 2; ++sK) { const bf16_t* qp = Qw + 64 * sK + 32 * hi; unsigned w[8];
; #pragma unroll
;           for (int c = 0; c < 4; ++c) { const u32x4 v = *(const u32x4*)(qp + 8 * c);
;               w[2 * c] = pk4_fp8(bflo(v.x) * QC, bfhi(v.x) * QC, bflo(v.y) * QC, bfhi(v.y) * QC); w[2 * c + 1] = pk4_fp8(bflo(v.z) * QC, bfhi(v.z) * QC, bflo(v.w) * QC, bfhi(v.w) * QC); }
;           qf[sK] = (i32x8){(int)w[0], (int)w[1], (int)w[2], (int)w[3], (int)w[4], (int)w[5], (int)w[6], (int)w[7]}; }
; __global__ void __launch_bounds__(NTHR, 2) fwd(Params p) {
;     ...
;                 for (int u = vcu; u < 1024; u += G) {
;                     __syncthreads();
;                     const int b = u >> 7, qb = u & 15, kvh = (u >> 6) & 1, gq = (u >> 4) & 3, h = kvh * 4 + gq;
;                     if constexpr (F8_ATTA) {
;                         d8::D8Args a; a.Q = Hx + (size_t)(b * SEQ + 256 * qb) * IN0 + h * 128; a.ldq = IN0;
;                         a.K8 = ws + WS_WGU0 + 64 * MiB + (size_t)b * SEQ * 256 + kvh * 128; a.ldk = 256; a.Kr8 = nullptr;
;                         a.Vt8 = ws + WS_WGU0 + 72 * MiB + (size_t)(b * 2 + kvh) * 128 * SEQ; a.ldvt = SEQ;
;                         { const size_t eo = (size_t)(b * SEQ + 256 * qb) * DM + h * 128; a.O = F8_OUT ? (bf16_t*)((unsigned char*)Oat + eo) : Oat + eo; } a.ldo = DM; a.seq = SEQ; a.pos0 = 0;
.LBB0_516:
	s_ashr_i32 s24, s42, 7
	s_lshl_b32 s1, s42, 8
	s_lshl_b32 s0, s24, 12
	s_and_b32 s1, s1, 0xf00
	s_or_b32 s2, s0, s1
	s_bfe_u32 s3, s42, 0x10006
	s_mul_i32 s1, s2, 0x2400
	s_mul_hi_i32 s0, s2, 0x2400
	s_add_u32 s1, s68, s1
	s_addc_u32 s15, s69, s0
	s_lshl_b32 s23, s42, 3
	s_lshl_b32 s0, s3, 9
	s_and_b32 s23, s23, 0x180
	s_or_b32 s43, s0, s23
	s_lshl_b32 s0, s43, 1
	s_add_u32 s0, s1, s0
	s_addc_u32 s1, s15, 0
	s_ashr_i32 s25, s24, 31
	s_lshl_b64 s[34:35], s[24:25], 20
	s_add_u32 s15, s6, s34
	s_addc_u32 s23, s7, s35
	s_lshl_b32 s25, s3, 7
	s_add_u32 s28, s15, s25
	s_addc_u32 s29, s23, 0
	s_lshl_b32 s15, s24, 1
	s_or_b32 s24, s15, s3
	s_ashr_i32 s25, s24, 31
	s_waitcnt vmcnt(0)
	s_barrier
	s_lshl_b64 s[24:25], s[24:25], 19
	v_mbcnt_lo_u32_b32 v16, -1, 0
	v_mbcnt_hi_u32_b32 v16, -1, v16
	s_add_u32 s24, s8, s24
	v_add_u32_e32 v0, s5, v16
	s_addc_u32 s25, s9, s25
	v_readfirstlane_b32 s3, v0
	s_ashr_i32 s23, s3, 6
	v_bfe_u32 v0, v16, 3, 3
	v_lshl_or_b32 v1, s23, 3, v0
	s_lshl_b32 s33, s23, 2
	v_lshrrev_b32_e32 v1, 1, v1
	s_and_b32 s52, s33, 12
	s_ashr_i32 s33, s3, 4
	v_xor_b32_e32 v2, v1, v16
	v_and_b32_e32 v245, 63, v16
	v_and_b32_e32 v17, 32, v16
	s_and_b32 s33, s33, -16
	v_lshlrev_b32_e32 v2, 4, v2
	s_lshl_b32 s53, s23, 4
	v_bfe_u32 v238, v16, 2, 4
	v_bfe_u32 v244, v245, 3, 2
	v_add_u32_e32 v239, s33, v17
	v_and_b32_e32 v232, 0x70, v2
	v_or_b32_e32 v2, s53, v238
	v_or3_b32 v0, v244, s52, v239
	v_ashrrev_i32_e32 v3, 31, v2
	v_ashrrev_i32_e32 v1, 31, v0
	v_lshlrev_b64 v[2:3], 12, v[2:3]
	v_lshlrev_b64 v[0:1], 8, v[0:1]
	v_lshl_add_u64 v[2:3], s[24:25], 0, v[2:3]
	s_lshl_b32 s24, s23, 10
	v_lshl_add_u64 v[0:1], s[28:29], 0, v[0:1]
	v_lshlrev_b32_e32 v4, 4, v16
	s_add_i32 s44, s24, 0
	v_lshl_add_u64 v[0:1], v[0:1], 0, v[232:233]
	v_bitop3_b32 v234, v4, 48, v16 bitop3:0x48
	v_mov_b32_e32 v235, v233
	s_add_i32 s45, s44, 0x12000
	s_mov_b32 m0, s44
	v_lshl_add_u64 v[2:3], v[2:3], 0, v[234:235]
	global_load_lds_dwordx4 v[0:1], off
	s_mov_b32 m0, s45
	v_lshl_add_u64 v[4:5], v[0:1], 0, s[94:95]
	global_load_lds_dwordx4 v[2:3], off
	s_add_i32 m0, s44, 0x2000
	s_mov_b64 s[24:25], 0xc000
	global_load_lds_dwordx4 v[4:5], off
	v_lshl_add_u64 v[4:5], v[2:3], 0, 64
	s_add_i32 m0, s44, 0x14000
	v_and_b32_e32 v240, 31, v16
	global_load_lds_dwordx4 v[4:5], off
	v_lshl_add_u64 v[4:5], v[0:1], 0, s[56:57]
	s_add_i32 m0, s44, 0x4000
	v_lshl_add_u64 v[0:1], v[0:1], 0, s[24:25]
	global_load_lds_dwordx4 v[4:5], off
	v_lshl_add_u64 v[4:5], v[2:3], 0, s[20:21]
	s_add_i32 m0, s44, 0x16000
	s_mov_b64 s[24:25], 0xc0
	global_load_lds_dwordx4 v[4:5], off
	s_add_i32 m0, s44, 0x6000
	s_nop 0
	global_load_lds_dwordx4 v[0:1], off
	v_lshl_add_u64 v[0:1], v[2:3], 0, s[24:25]
	s_add_i32 m0, s44, 0x18000
	s_nop 0
	global_load_lds_dwordx4 v[0:1], off
	v_lshl_or_b32 v2, s23, 5, v240
	v_mov_b64_e32 v[0:1], s[0:1]
	s_movk_i32 s0, 0x2400
	v_mad_i64_i32 v[0:1], s[0:1], v2, s0, v[0:1]
	v_lshlrev_b32_e32 v2, 1, v17
	v_mov_b32_e32 v3, v233
	v_lshl_add_u64 v[12:13], v[0:1], 0, v[2:3]
	global_load_dwordx4 v[0:3], v[12:13], off offset:48
	global_load_dwordx4 v[4:7], v[12:13], off offset:32
	global_load_dwordx4 v[8:11], v[12:13], off offset:16
	global_load_dwordx4 v[18:21], v[12:13], off
	global_load_dwordx4 v[40:43], v[12:13], off offset:176
	global_load_dwordx4 v[44:47], v[12:13], off offset:160
	global_load_dwordx4 v[48:51], v[12:13], off offset:144
	global_load_dwordx4 v[52:55], v[12:13], off offset:128
	s_waitcnt vmcnt(0)
	v_lshlrev_b32_e32 v14, 16, v18
	v_mul_f32_e32 v216, 0x3e0293ee, v14
	v_and_b32_e32 v14, 0xffff0000, v18
	v_mul_f32_e32 v14, 0x3e0293ee, v14
	v_cvt_pk_fp8_f32 v216, v216, v14
	v_lshlrev_b32_e32 v14, 16, v20
	v_mul_f32_e32 v217, 0x3e0293ee, v14
	v_and_b32_e32 v14, 0xffff0000, v20
	v_mul_f32_e32 v14, 0x3e0293ee, v14
	v_cvt_pk_fp8_f32 v217, v217, v14
	v_lshlrev_b32_e32 v14, 16, v8
	v_and_b32_e32 v8, 0xffff0000, v8
	v_mul_f32_e32 v218, 0x3e0293ee, v14
	v_mul_f32_e32 v8, 0x3e0293ee, v8
	v_cvt_pk_fp8_f32 v218, v218, v8
	v_lshlrev_b32_e32 v8, 16, v10
	v_mul_f32_e32 v219, 0x3e0293ee, v8
	v_and_b32_e32 v8, 0xffff0000, v10
	v_mul_f32_e32 v8, 0x3e0293ee, v8
	v_cvt_pk_fp8_f32 v219, v219, v8
	v_lshlrev_b32_e32 v8, 16, v4
	v_and_b32_e32 v4, 0xffff0000, v4
	v_mul_f32_e32 v220, 0x3e0293ee, v8
	v_mul_f32_e32 v4, 0x3e0293ee, v4
	v_cvt_pk_fp8_f32 v220, v220, v4
	v_lshlrev_b32_e32 v4, 16, v6
	v_mul_f32_e32 v221, 0x3e0293ee, v4
	v_and_b32_e32 v4, 0xffff0000, v6
	v_mul_f32_e32 v4, 0x3e0293ee, v4
	v_cvt_pk_fp8_f32 v221, v221, v4
	v_lshlrev_b32_e32 v4, 16, v0
	v_and_b32_e32 v0, 0xffff0000, v0
	v_mul_f32_e32 v222, 0x3e0293ee, v4
	v_mul_f32_e32 v0, 0x3e0293ee, v0
	v_cvt_pk_fp8_f32 v222, v222, v0
	v_lshlrev_b32_e32 v0, 16, v2
	v_mul_f32_e32 v223, 0x3e0293ee, v0
	v_and_b32_e32 v0, 0xffff0000, v2
	v_mul_f32_e32 v0, 0x3e0293ee, v0
	v_lshlrev_b32_e32 v15, 16, v19
	v_and_b32_e32 v18, 0xffff0000, v19
	v_lshlrev_b32_e32 v14, 16, v9
	v_and_b32_e32 v9, 0xffff0000, v9
	v_lshlrev_b32_e32 v8, 16, v5
	v_and_b32_e32 v5, 0xffff0000, v5
	v_lshlrev_b32_e32 v4, 16, v1
	v_and_b32_e32 v1, 0xffff0000, v1
	v_cvt_pk_fp8_f32 v223, v223, v0
	v_mul_f32_e32 v15, 0x3e0293ee, v15
	v_mul_f32_e32 v18, 0x3e0293ee, v18
	v_mul_f32_e32 v14, 0x3e0293ee, v14
	v_mul_f32_e32 v9, 0x3e0293ee, v9
	v_mul_f32_e32 v8, 0x3e0293ee, v8
	v_mul_f32_e32 v5, 0x3e0293ee, v5
	v_mul_f32_e32 v4, 0x3e0293ee, v4
	v_mul_f32_e32 v1, 0x3e0293ee, v1
	v_cvt_pk_fp8_f32 v216, v15, v18 op_sel:[0,0,1]
	v_lshlrev_b32_e32 v15, 16, v21
	v_and_b32_e32 v18, 0xffff0000, v21
	v_cvt_pk_fp8_f32 v218, v14, v9 op_sel:[0,0,1]
	v_lshlrev_b32_e32 v9, 16, v11
	v_and_b32_e32 v10, 0xffff0000, v11
	v_cvt_pk_fp8_f32 v220, v8, v5 op_sel:[0,0,1]
	v_lshlrev_b32_e32 v5, 16, v7
	v_and_b32_e32 v6, 0xffff0000, v7
	v_cvt_pk_fp8_f32 v222, v4, v1 op_sel:[0,0,1]
	v_lshlrev_b32_e32 v1, 16, v3
	v_and_b32_e32 v2, 0xffff0000, v3
	v_mul_f32_e32 v15, 0x3e0293ee, v15
	v_mul_f32_e32 v18, 0x3e0293ee, v18
	v_mul_f32_e32 v9, 0x3e0293ee, v9
	v_mul_f32_e32 v10, 0x3e0293ee, v10
	v_mul_f32_e32 v5, 0x3e0293ee, v5
	v_mul_f32_e32 v6, 0x3e0293ee, v6
	v_mul_f32_e32 v1, 0x3e0293ee, v1
	v_mul_f32_e32 v2, 0x3e0293ee, v2
	v_cvt_pk_fp8_f32 v217, v15, v18 op_sel:[0,0,1]
	v_cvt_pk_fp8_f32 v219, v9, v10 op_sel:[0,0,1]
	v_cvt_pk_fp8_f32 v221, v5, v6 op_sel:[0,0,1]
	v_cvt_pk_fp8_f32 v223, v1, v2 op_sel:[0,0,1]
	v_mov_b64_e32 v[0:1], v[40:41]
	v_mov_b64_e32 v[2:3], v[42:43]
	v_mov_b64_e32 v[4:5], v[44:45]
	v_mov_b64_e32 v[6:7], v[46:47]
	v_mov_b64_e32 v[8:9], v[48:49]
	v_mov_b64_e32 v[10:11], v[50:51]
	v_mov_b64_e32 v[12:13], v[52:53]
	v_mov_b64_e32 v[14:15], v[54:55]
	s_waitcnt vmcnt(0)
; __device__ __forceinline__ float bflo(unsigned w) { return __uint_as_float(w << 16); }
; __device__ __forceinline__ float bfhi(unsigned w) { return __uint_as_float(w & 0xffff0000u); }
; #define RESC8(al) do { if (__any((al) < 1.f)) { if (hi == 0) al_l[r32] = (al); asm volatile("s_waitcnt lgkmcnt(0)" ::: "memory"); \
;     _Pragma("unroll") for (int d = 0; d < 4; ++d) _Pragma("unroll") for (int r = 0; r < 16; ++r) o[d][r] *= al_l[da::crow(r, hi)]; } } while (0)
; #define RESC8(al) do { if (__any((al) < 1.f)) { if (hi == 0) al_l[r32] = (al); asm volatile("s_waitcnt lgkmcnt(0)" ::: "memory"); \
;     _Pragma("unroll") for (int d = 0; d < 4; ++d) _Pragma("unroll") for (int r = 0; r < 16; ++r) o[d][r] *= al_l[da::crow(r, hi)]; \
;     if constexpr (LSUM) { _Pragma("unroll") for (int r = 0; r < 16; ++r) lacc[r] *= al_l[da::crow(r, hi)]; } } } while (0)
; #define D8Qm(P0, P1, b) qkt8d<NKS, MACC>(P0, P1, mneg, ldsl, kb0 + (b) * K8_BYTES, rb0 + (b) * KR8_BYTES, qf)
; #define D8Pm(FIRST, P0, P1, AL) do { if constexpr (MACC) partialSM8<FIRST, (NKS == 3)>(P0, P1, m_reg, mneg, AL); else partialSM8z<NKS>(P0, P1, m_reg, AL); } while (0)
; #define D8_TOP() do { asm volatile("s_waitcnt vmcnt(0)" ::: "memory"); __syncthreads(); } while (0)
; template <int NKS, bool MACC>
; __device__ __forceinline__ void attn_dense8_dma(int wv, const D8Args a, LAS unsigned char* ldsl) {
;     ...
;           for (int c = 0; c < 4; ++c) { const u32x4 v = *(const u32x4*)(qp + 8 * c);
;               w[2 * c] = pk4_fp8(bflo(v.x) * QC, bfhi(v.x) * QC, bflo(v.y) * QC, bfhi(v.y) * QC); w[2 * c + 1] = pk4_fp8(bflo(v.z) * QC, bfhi(v.z) * QC, bflo(v.w) * QC, bfhi(v.w) * QC); }
;           qf[sK] = (i32x8){(int)w[0], (int)w[1], (int)w[2], (int)w[3], (int)w[4], (int)w[5], (int)w[6], (int)w[7]}; }
;     ...
;     float* al_l = (float*)(lds + DM_WS) + wid * 64 + 32;
;     const int kb0 = DM_K + r32 * 128 + ((((r32 >> 1) & 7) << 4) ^ (32 * hi)), rb0 = DM_KR + r32 * 64 + ((((r32 >> 2) & 3) << 4) ^ (32 * hi)), vb0 = DM_VT + r32 * 64 + ((((r32 >> 2) & 3) << 4) ^ (32 * hi));
;     f32x16 pA0, pA1, pB0, pB1; float alA, alB; i32x8 pa;
;     const int NS = a.seq / 128;
;     D8_TOP();
;     D8Qm(pA0, pA1, 0); D8Pm(true, pA0, pA1, alA); RESC8(alA);
	v_lshlrev_b32_e32 v18, 16, v12
	v_and_b32_e32 v12, 0xffff0000, v12
	v_mul_f32_e32 v224, 0x3e0293ee, v18
	v_mul_f32_e32 v12, 0x3e0293ee, v12
	v_cvt_pk_fp8_f32 v224, v224, v12
	v_lshlrev_b32_e32 v12, 16, v14
	v_mul_f32_e32 v225, 0x3e0293ee, v12
	v_and_b32_e32 v12, 0xffff0000, v14
	v_mul_f32_e32 v12, 0x3e0293ee, v12
	v_cvt_pk_fp8_f32 v225, v225, v12
	v_lshlrev_b32_e32 v12, 16, v8
	v_and_b32_e32 v8, 0xffff0000, v8
	v_mul_f32_e32 v226, 0x3e0293ee, v12
	v_mul_f32_e32 v8, 0x3e0293ee, v8
	v_cvt_pk_fp8_f32 v226, v226, v8
	v_lshlrev_b32_e32 v8, 16, v10
	v_mul_f32_e32 v227, 0x3e0293ee, v8
	v_and_b32_e32 v8, 0xffff0000, v10
	v_mul_f32_e32 v8, 0x3e0293ee, v8
	v_cvt_pk_fp8_f32 v227, v227, v8
	v_lshlrev_b32_e32 v8, 16, v4
	v_and_b32_e32 v4, 0xffff0000, v4
	v_mul_f32_e32 v228, 0x3e0293ee, v8
	v_mul_f32_e32 v4, 0x3e0293ee, v4
	v_cvt_pk_fp8_f32 v228, v228, v4
	v_lshlrev_b32_e32 v4, 16, v6
	v_mul_f32_e32 v229, 0x3e0293ee, v4
	v_and_b32_e32 v4, 0xffff0000, v6
	v_mul_f32_e32 v4, 0x3e0293ee, v4
	v_cvt_pk_fp8_f32 v229, v229, v4
	v_lshlrev_b32_e32 v4, 16, v0
	v_and_b32_e32 v0, 0xffff0000, v0
	v_mul_f32_e32 v230, 0x3e0293ee, v4
	v_mul_f32_e32 v0, 0x3e0293ee, v0
	v_cvt_pk_fp8_f32 v230, v230, v0
	v_lshlrev_b32_e32 v0, 16, v2
	v_mul_f32_e32 v231, 0x3e0293ee, v0
	v_and_b32_e32 v0, 0xffff0000, v2
	v_mul_f32_e32 v0, 0x3e0293ee, v0
	v_lshlrev_b32_e32 v18, 16, v13
	v_and_b32_e32 v13, 0xffff0000, v13
	v_lshlrev_b32_e32 v12, 16, v9
	v_and_b32_e32 v9, 0xffff0000, v9
	v_lshlrev_b32_e32 v8, 16, v5
	v_and_b32_e32 v5, 0xffff0000, v5
	v_lshlrev_b32_e32 v4, 16, v1
	v_and_b32_e32 v1, 0xffff0000, v1
	v_cvt_pk_fp8_f32 v231, v231, v0
	v_mul_f32_e32 v18, 0x3e0293ee, v18
	v_mul_f32_e32 v13, 0x3e0293ee, v13
	v_mul_f32_e32 v12, 0x3e0293ee, v12
	v_mul_f32_e32 v9, 0x3e0293ee, v9
	v_mul_f32_e32 v8, 0x3e0293ee, v8
	v_mul_f32_e32 v5, 0x3e0293ee, v5
	v_mul_f32_e32 v4, 0x3e0293ee, v4
	v_mul_f32_e32 v1, 0x3e0293ee, v1
	v_cvt_pk_fp8_f32 v224, v18, v13 op_sel:[0,0,1]
	v_lshlrev_b32_e32 v13, 16, v15
	v_and_b32_e32 v14, 0xffff0000, v15
	v_cvt_pk_fp8_f32 v226, v12, v9 op_sel:[0,0,1]
	v_lshlrev_b32_e32 v9, 16, v11
	v_and_b32_e32 v10, 0xffff0000, v11
	v_cvt_pk_fp8_f32 v228, v8, v5 op_sel:[0,0,1]
	v_lshlrev_b32_e32 v5, 16, v7
	v_and_b32_e32 v6, 0xffff0000, v7
	v_cvt_pk_fp8_f32 v230, v4, v1 op_sel:[0,0,1]
	v_lshlrev_b32_e32 v1, 16, v3
	v_and_b32_e32 v2, 0xffff0000, v3
	v_mul_f32_e32 v13, 0x3e0293ee, v13
	v_mul_f32_e32 v14, 0x3e0293ee, v14
	v_mul_f32_e32 v9, 0x3e0293ee, v9
	v_mul_f32_e32 v10, 0x3e0293ee, v10
	v_mul_f32_e32 v5, 0x3e0293ee, v5
	v_mul_f32_e32 v6, 0x3e0293ee, v6
	v_mul_f32_e32 v1, 0x3e0293ee, v1
	v_mul_f32_e32 v2, 0x3e0293ee, v2
	v_cvt_pk_fp8_f32 v225, v13, v14 op_sel:[0,0,1]
	v_cvt_pk_fp8_f32 v227, v9, v10 op_sel:[0,0,1]
	v_cvt_pk_fp8_f32 v229, v5, v6 op_sel:[0,0,1]
	v_cvt_pk_fp8_f32 v231, v1, v2 op_sel:[0,0,1]
	v_lshlrev_b32_e32 v0, 3, v16
	v_lshlrev_b32_e32 v8, 7, v240
	v_and_b32_e32 v1, 0x70, v0
	v_bitop3_b32 v9, v0, v17, s89 bitop3:0x6c
	v_bitop3_b32 v248, v1, v8, v17 bitop3:0xde
	v_lshlrev_b32_e32 v0, 2, v16
	s_movk_i32 s0, 0x50
	v_lshlrev_b32_e32 v80, 6, v240
	v_and_b32_e32 v1, 48, v0
	v_add_u32_e32 v65, 0, v248
	v_xad_u32 v67, v248, 64, 0
	v_bitop3_b32 v8, v9, s0, v8 bitop3:0x36
	v_bitop3_b32 v81, v0, v17, 48 bitop3:0x6c
	v_bitop3_b32 v235, v1, v80, v17 bitop3:0xde
	s_waitcnt vmcnt(0)
	s_waitcnt lgkmcnt(0)
	s_barrier
	v_xad_u32 v66, v248, 16, 0
	ds_read_b128 v[0:3], v65
	ds_read_b128 v[48:51], v65 offset:4096
	ds_read_b128 v[4:7], v66
	ds_read_b128 v[52:55], v66 offset:4096
	v_add_u32_e32 v68, 0, v8
	ds_read_b128 v[8:11], v67
	ds_read_b128 v[56:59], v67 offset:4096
	ds_read_b128 v[12:15], v68
	ds_read_b128 v[60:63], v68 offset:4096
	s_waitcnt lgkmcnt(0)
	v_or_b32_e32 v249, 0x12000, v235
	v_readlane_b32 s72, v254, 31
	v_readlane_b32 s73, v254, 32
	v_readlane_b32 s74, v254, 33
	v_readlane_b32 s75, v254, 34
	v_readlane_b32 s76, v254, 35
	v_readlane_b32 s77, v254, 36
	v_readlane_b32 s78, v254, 37
	v_readlane_b32 s79, v254, 38
	v_readlane_b32 s80, v254, 39
	v_readlane_b32 s81, v254, 40
	v_readlane_b32 s82, v254, 41
	v_readlane_b32 s83, v254, 42
	v_readlane_b32 s84, v254, 43
	v_readlane_b32 s85, v254, 44
	v_readlane_b32 s86, v254, 45
	v_readlane_b32 s87, v254, 46
	v_mov_b64_e32 v[32:33], s[72:73]
	v_mov_b64_e32 v[34:35], s[74:75]
	v_mov_b64_e32 v[36:37], s[76:77]
	v_mov_b64_e32 v[38:39], s[78:79]
	v_mov_b64_e32 v[40:41], s[80:81]
	v_mov_b64_e32 v[42:43], s[82:83]
	v_mov_b64_e32 v[44:45], s[84:85]
	v_mov_b64_e32 v[46:47], s[86:87]
	s_waitcnt lgkmcnt(5)
	v_mfma_f32_32x32x64_f8f6f4 v[16:31], v[0:7], v[216:223], v[32:47]
	s_waitcnt lgkmcnt(1)
	v_mfma_f32_32x32x64_f8f6f4 v[16:31], v[8:15], v[224:231], v[16:31]
	v_mfma_f32_32x32x64_f8f6f4 v[0:15], v[48:55], v[216:223], v[32:47]
	s_waitcnt lgkmcnt(0)
; #define SBAR() __builtin_amdgcn_sched_barrier(0)
; #define SBAR() __builtin_amdgcn_sched_barrier(0)
; #define RESC8(al) do { if (__any((al) < 1.f)) { if (hi == 0) al_l[r32] = (al); asm volatile("s_waitcnt lgkmcnt(0)" ::: "memory"); \
;     _Pragma("unroll") for (int d = 0; d < 4; ++d) _Pragma("unroll") for (int r = 0; r < 16; ++r) o[d][r] *= al_l[da::crow(r, hi)]; } } while (0)
; #define RESC8(al) do { if (__any((al) < 1.f)) { if (hi == 0) al_l[r32] = (al); asm volatile("s_waitcnt lgkmcnt(0)" ::: "memory"); \
;     _Pragma("unroll") for (int d = 0; d < 4; ++d) _Pragma("unroll") for (int r = 0; r < 16; ++r) o[d][r] *= al_l[da::crow(r, hi)]; \
;     if constexpr (LSUM) { _Pragma("unroll") for (int r = 0; r < 16; ++r) lacc[r] *= al_l[da::crow(r, hi)]; } } } while (0)
; template <bool FIRST, bool SPLAT = false>
; __device__ __forceinline__ void partialSM8(f32x16& p0, f32x16& p1, float& m_reg, f32x16& mneg, float& alpha) {
;     float pmax = p0[0];
; #pragma unroll
;     for (int r = 1; r < 16; ++r) pmax = fmaxf(pmax, p0[r]);
; #pragma unroll
;     for (int r = 0; r < 16; ++r) pmax = fmaxf(pmax, p1[r]);
;     { auto rr = __builtin_amdgcn_permlane32_swap(__float_as_uint(pmax), __float_as_uint(pmax), false, false);
;       pmax = fmaxf(__uint_as_float(rr[0]), __uint_as_float(rr[1])); }
;     if (!FIRST && __builtin_expect(__all(pmax <= THR8 * LOG2E), 1)) { alpha = 1.f; }
;     else { const float delta = FIRST ? pmax : fmaxf(pmax, 0.f); alpha = FIRST ? 1.f : __builtin_amdgcn_exp2f(-delta); m_reg += delta;
; #pragma unroll
;         for (int r = 0; r < 16; ++r) { p0[r] -= delta; p1[r] -= delta; }
;         if constexpr (!SPLAT) { const float nm = -m_reg;
; #pragma unroll
;             for (int r = 0; r < 16; ++r) mneg[r] = nm; } }
;     if constexpr (SPLAT) { float nm = -m_reg; asm volatile("" : "+v"(nm));
; #pragma unroll
;         for (int r = 0; r < 16; ++r) mneg[r] = nm; }
; #pragma unroll
;     for (int r = 0; r < 16; ++r) p0[r] = __builtin_amdgcn_exp2f(p0[r]);
; }
; template <int NKS, bool MACC>
; __device__ __forceinline__ void attn_dense8_dma(int wv, const D8Args a, LAS unsigned char* ldsl) {
;     ...
;     D8Qm(pA0, pA1, 0); D8Pm(true, pA0, pA1, alA); RESC8(alA);
;     SBAR(); D8Qm(pB0, pB1, 1);
;     D8Fm(pA0, pA1, alA); SBAR();
;     D8Vm(0); D8Pm(false, pB0, pB1, alB);
	v_mfma_f32_32x32x64_f8f6f4 v[0:15], v[56:63], v[224:231], v[0:15]
	s_nop 15
	s_nop 1
	v_max_f32_e32 v32, v17, v17
	v_max_f32_e32 v33, v16, v16
	v_max_f32_e32 v32, v33, v32
	v_max3_f32 v32, v32, v18, v19
	v_max3_f32 v32, v32, v20, v21
	v_max3_f32 v32, v32, v22, v23
	v_max3_f32 v32, v32, v24, v25
	v_max3_f32 v32, v32, v26, v27
	v_max3_f32 v32, v32, v28, v29
	v_max3_f32 v32, v32, v30, v31
	v_max3_f32 v32, v32, v0, v1
	v_max3_f32 v32, v32, v2, v3
	v_max3_f32 v32, v32, v4, v5
	v_max3_f32 v32, v32, v6, v7
	v_max3_f32 v32, v32, v8, v9
	v_max3_f32 v32, v32, v10, v11
	v_max3_f32 v32, v32, v12, v13
	v_max3_f32 v32, v32, v14, v15
	v_mov_b32_e32 v33, v32
	s_nop 1
	v_permlane32_swap_b32_e32 v32, v33
	v_max_f32_e32 v33, v33, v33
	v_max_f32_e32 v32, v32, v32
	v_max_f32_e32 v32, v32, v33
	v_sub_f32_e32 v16, v16, v32
	v_sub_f32_e32 v37, v1, v32
	v_sub_f32_e32 v1, v18, v32
	v_sub_f32_e32 v39, v3, v32
	v_sub_f32_e32 v3, v20, v32
	v_sub_f32_e32 v36, v0, v32
	v_exp_f32_e32 v0, v16
	v_exp_f32_e32 v51, v1
	v_exp_f32_e32 v1, v3
	v_add_f32_e32 v236, 0, v32
	v_sub_f32_e32 v17, v17, v32
	v_sub_f32_e32 v38, v2, v32
	v_sub_f32_e32 v2, v19, v32
	v_sub_f32_e32 v40, v4, v32
	v_sub_f32_e32 v4, v21, v32
	v_sub_f32_e32 v41, v5, v32
	v_sub_f32_e32 v5, v22, v32
	v_sub_f32_e32 v42, v6, v32
	v_sub_f32_e32 v6, v23, v32
	v_sub_f32_e32 v43, v7, v32
	v_sub_f32_e32 v7, v24, v32
	v_sub_f32_e32 v44, v8, v32
	v_sub_f32_e32 v8, v25, v32
	v_sub_f32_e32 v45, v9, v32
	v_sub_f32_e32 v9, v26, v32
	v_sub_f32_e32 v46, v10, v32
	v_sub_f32_e32 v10, v27, v32
	v_sub_f32_e32 v47, v11, v32
	v_sub_f32_e32 v11, v28, v32
	v_sub_f32_e32 v48, v12, v32
	v_sub_f32_e32 v12, v29, v32
	v_sub_f32_e32 v49, v13, v32
	v_sub_f32_e32 v13, v30, v32
	v_sub_f32_e32 v18, v31, v32
	v_xor_b32_e32 v64, 0x80000000, v236
	v_exp_f32_e32 v50, v17
	v_exp_f32_e32 v52, v2
	v_exp_f32_e32 v53, v4
	v_exp_f32_e32 v54, v5
	v_exp_f32_e32 v55, v6
	v_exp_f32_e32 v2, v7
	v_exp_f32_e32 v56, v8
	v_exp_f32_e32 v57, v9
	v_exp_f32_e32 v58, v10
	v_exp_f32_e32 v3, v11
	v_exp_f32_e32 v59, v12
	v_exp_f32_e32 v60, v13
	v_exp_f32_e32 v61, v18
	v_sub_f32_e32 v62, v14, v32
	v_sub_f32_e32 v63, v15, v32
	ds_read_b128 v[4:7], v65 offset:8192
	ds_read_b128 v[12:15], v65 offset:12288
	ds_read_b128 v[8:11], v66 offset:8192
	ds_read_b128 v[16:19], v66 offset:12288
	ds_read_b128 v[20:23], v67 offset:8192
	ds_read_b128 v[28:31], v67 offset:12288
	ds_read_b128 v[24:27], v68 offset:8192
	ds_read_b128 v[32:35], v68 offset:12288
	s_waitcnt lgkmcnt(0)
	v_mov_b32_e32 v65, v64
	v_mov_b32_e32 v66, v64
	v_mov_b32_e32 v67, v64
	v_mov_b32_e32 v68, v64
	v_mov_b32_e32 v69, v64
	v_mov_b32_e32 v70, v64
	v_mov_b32_e32 v71, v64
	v_mov_b32_e32 v72, v64
	v_mov_b32_e32 v73, v64
	v_mov_b32_e32 v74, v64
	v_mov_b32_e32 v75, v64
	v_mov_b32_e32 v76, v64
	v_mov_b32_e32 v77, v64
	v_mov_b32_e32 v78, v64
	v_mov_b32_e32 v79, v64
	s_waitcnt lgkmcnt(5)
	v_mfma_f32_32x32x64_f8f6f4 v[112:127], v[4:11], v[216:223], v[64:79]
	s_waitcnt lgkmcnt(4)
	v_mfma_f32_32x32x64_f8f6f4 v[96:111], v[12:19], v[216:223], v[64:79]
	v_exp_f32_e32 v4, v36
	v_exp_f32_e32 v8, v37
	v_exp_f32_e32 v5, v40
	v_exp_f32_e32 v11, v41
	v_exp_f32_e32 v6, v44
	v_exp_f32_e32 v14, v45
	v_exp_f32_e32 v7, v48
	v_exp_f32_e32 v17, v49
	v_cvt_pk_fp8_f32 v0, v0, v50
	v_cvt_pk_fp8_f32 v1, v1, v53
	v_exp_f32_e32 v9, v38
	v_exp_f32_e32 v10, v39
	v_exp_f32_e32 v12, v42
	v_exp_f32_e32 v13, v43
	v_exp_f32_e32 v15, v46
	v_exp_f32_e32 v16, v47
	v_exp_f32_e32 v18, v62
	v_exp_f32_e32 v19, v63
	v_cvt_pk_fp8_f32 v2, v2, v56
	v_cvt_pk_fp8_f32 v3, v3, v59
	v_cvt_pk_fp8_f32 v0, v51, v52 op_sel:[0,0,1]
	v_cvt_pk_fp8_f32 v1, v54, v55 op_sel:[0,0,1]
	v_cvt_pk_fp8_f32 v4, v4, v8
	v_cvt_pk_fp8_f32 v5, v5, v11
	v_cvt_pk_fp8_f32 v6, v6, v14
	v_cvt_pk_fp8_f32 v7, v7, v17
	s_waitcnt lgkmcnt(1)
	v_mfma_f32_32x32x64_f8f6f4 v[112:127], v[20:27], v[224:231], v[112:127]
	v_cvt_pk_fp8_f32 v2, v57, v58 op_sel:[0,0,1]
	v_cvt_pk_fp8_f32 v3, v60, v61 op_sel:[0,0,1]
	v_cvt_pk_fp8_f32 v4, v9, v10 op_sel:[0,0,1]
	v_cvt_pk_fp8_f32 v5, v12, v13 op_sel:[0,0,1]
	v_cvt_pk_fp8_f32 v6, v15, v16 op_sel:[0,0,1]
	v_cvt_pk_fp8_f32 v7, v18, v19 op_sel:[0,0,1]
	s_waitcnt lgkmcnt(0)
	v_mfma_f32_32x32x64_f8f6f4 v[96:111], v[28:35], v[224:231], v[96:111]
	s_mov_b32 s0, 0x12010
	v_bitop3_b32 v8, v81, s0, v80 bitop3:0x36
	v_add_u32_e32 v251, 0, v249
	v_add_u32_e32 v36, 0, v8
	ds_read_b128 v[8:11], v251
	ds_read_b128 v[16:19], v251 offset:2048
	ds_read_b128 v[12:15], v36
	ds_read_b128 v[20:23], v36 offset:2048
	ds_read_b128 v[24:27], v251 offset:4096
	ds_read_b128 v[32:35], v251 offset:6144
	ds_read_b128 v[28:31], v36 offset:4096
	ds_read_b128 v[36:39], v36 offset:6144
	s_waitcnt lgkmcnt(0)
	v_mov_b32_e32 v209, v208
	v_mov_b32_e32 v210, v208
	v_mov_b32_e32 v211, v208
	v_mov_b32_e32 v212, v208
	v_mov_b32_e32 v213, v208
	v_mov_b32_e32 v214, v208
	v_mov_b32_e32 v215, v208
	s_waitcnt lgkmcnt(5)
	v_mfma_f32_32x32x64_f8f6f4 v[128:143], v[0:7], v[8:15], 0
	s_waitcnt lgkmcnt(4)
	v_mfma_f32_32x32x64_f8f6f4 v[144:159], v[0:7], v[16:23], 0
	s_waitcnt lgkmcnt(1)
	v_mfma_f32_32x32x64_f8f6f4 v[160:175], v[0:7], v[24:31], 0
	s_waitcnt lgkmcnt(0)
	v_mfma_f32_32x32x64_f8f6f4 v[176:191], v[0:7], v[32:39], 0
	v_mfma_f32_32x32x64_f8f6f4 v[192:207], v[0:7], v[208:215], 0
	v_max_f32_e32 v0, v113, v113
	v_max_f32_e32 v1, v112, v112
	v_max_f32_e32 v0, v1, v0
	v_max3_f32 v0, v0, v114, v115
	v_max3_f32 v0, v0, v116, v117
	v_max3_f32 v0, v0, v118, v119
	v_max3_f32 v0, v0, v120, v121
	v_max3_f32 v0, v0, v122, v123
	v_max3_f32 v0, v0, v124, v125
	v_max3_f32 v0, v0, v126, v127
	v_max3_f32 v0, v0, v96, v97
	v_max3_f32 v0, v0, v98, v99
	v_max3_f32 v0, v0, v100, v101
	v_max3_f32 v0, v0, v102, v103
	v_max3_f32 v0, v0, v104, v105
	v_max3_f32 v0, v0, v106, v107
	v_max3_f32 v0, v0, v108, v109
	v_max3_f32 v0, v0, v110, v111
	v_mov_b32_e32 v1, v0
	s_nop 1
	v_permlane32_swap_b32_e32 v0, v1
	v_max_f32_e32 v1, v1, v1
	v_max_f32_e32 v0, v0, v0
	v_max_f32_e32 v1, v0, v1
	v_cmp_ge_f32_e32 vcc, s10, v1
	s_cmp_eq_u64 vcc, exec
	v_mov_b32_e32 v0, 1.0
	s_cbranch_scc0 .LBB0_540
